# attention loops: drop redundant movs/waits/canonicalizing max, negm phi copy moved to loop exit, exps into PV shadow
# baseline (speedup 1.0000x reference)
; DI void pv_all_sm(f32x16* o, int vb, bf16x8 pa0, bf16x8 pa1, bf16x8 pa2, bf16x8 pa3, f32x16& p0, f32x16& p1, float& m_ref, f32x16& negm, float& alpha) {
;     pv_one<0>(o[0], vb, pa0, pa1, pa2, pa3);
;     float pmax = p0[0];
; #pragma unroll
;     for (int r = 1; r < 16; ++r) pmax = fmaxf(pmax, p0[r]);
;     pv_one<1>(o[1], vb, pa0, pa1, pa2, pa3);
; #pragma unroll
;     for (int r = 0; r < 16; ++r) pmax = fmaxf(pmax, p1[r]);
;     { auto rr = __builtin_amdgcn_permlane32_swap(__float_as_uint(pmax), __float_as_uint(pmax), false, false); pmax = fmaxf(__uint_as_float(rr[0]), __uint_as_float(rr[1])); }
;     pv_one<2>(o[2], vb, pa0, pa1, pa2, pa3);
;     alpha = 1.f;
;     if (__builtin_expect(!__all(pmax <= THRL), 0)) {
;         const float dl = fmaxf(pmax, 0.f); m_ref += dl; alpha = __builtin_amdgcn_exp2f(-dl);
; #pragma unroll
;         for (int r = 0; r < 16; ++r) { p0[r] -= dl; p1[r] -= dl; }
; #pragma unroll
;         for (int r = 0; r < 16; ++r) negm[r] = -m_ref;
;     }
;     pv_one<3>(o[3], vb, pa0, pa1, pa2, pa3);
; #pragma unroll
;     for (int r = 0; r < 16; ++r) p0[r] = __builtin_amdgcn_exp2f(p0[r]);
; }
.LBB4_704:
	s_lshl_b32 s67, s65, 14
	v_add_u32_e32 v186, s67, v192
	ds_read_b64_tr_b16 v[64:65], v186 offset:0
	ds_read_b64_tr_b16 v[66:67], v186 offset:0x800
	ds_read_b64_tr_b16 v[68:69], v186 offset:0x1000
	ds_read_b64_tr_b16 v[70:71], v186 offset:0x1800
	ds_read_b64_tr_b16 v[72:73], v186 offset:0x2000
	ds_read_b64_tr_b16 v[74:75], v186 offset:0x2800
	ds_read_b64_tr_b16 v[76:77], v186 offset:0x3000
	ds_read_b64_tr_b16 v[78:79], v186 offset:0x3800
	s_waitcnt lgkmcnt(0)
	s_nop 0
	v_mfma_f32_32x32x16_bf16 v[32:47], v[64:67], v[96:99], v[32:47]
	v_max_f32_e32 v64, v128, v129
	v_max3_f32 v64, v64, v130, v131
	v_max3_f32 v64, v64, v132, v133
	v_max3_f32 v64, v64, v134, v135
	v_max3_f32 v64, v64, v136, v137
	v_mfma_f32_32x32x16_bf16 v[32:47], v[68:71], v[108:111], v[32:47]
	v_max3_f32 v64, v64, v138, v139
	v_max3_f32 v66, v64, v140, v141
	ds_read_b64_tr_b16 v[64:65], v186 offset:0x200
	v_max3_f32 v180, v66, v142, v143
	ds_read_b64_tr_b16 v[66:67], v186 offset:0xa00
	ds_read_b64_tr_b16 v[68:69], v186 offset:0x1200
	ds_read_b64_tr_b16 v[70:71], v186 offset:0x1a00
	v_mfma_f32_32x32x16_bf16 v[32:47], v[72:75], v[100:103], v[32:47]
	ds_read_b64_tr_b16 v[72:73], v186 offset:0x2200
	ds_read_b64_tr_b16 v[74:75], v186 offset:0x2a00
	ds_read_b64_tr_b16 v[214:215], v186 offset:0x3200
	ds_read_b64_tr_b16 v[216:217], v186 offset:0x3a00
	s_waitcnt lgkmcnt(0)
	v_mfma_f32_32x32x16_bf16 v[32:47], v[76:79], v[104:107], v[32:47]
	v_mfma_f32_32x32x16_bf16 v[48:63], v[64:67], v[96:99], v[48:63]
	v_max3_f32 v76, v180, v112, v113
	v_max3_f32 v64, v76, v114, v115
	ds_read_b64_tr_b16 v[66:67], v186 offset:0x400
	v_max3_f32 v64, v64, v116, v117
	v_max3_f32 v64, v64, v118, v119
	v_max3_f32 v64, v64, v120, v121
	v_max3_f32 v64, v64, v122, v123
	v_mfma_f32_32x32x16_bf16 v[48:63], v[68:71], v[108:111], v[48:63]
	ds_read_b64_tr_b16 v[68:69], v186 offset:0xc00
	ds_read_b64_tr_b16 v[70:71], v186 offset:0x1400
	v_max3_f32 v64, v64, v124, v125
	v_max3_f32 v64, v64, v126, v127
	v_mov_b32_e32 v65, v64
	s_nop 1
	v_permlane32_swap_b32_e32 v64, v65
	v_mfma_f32_32x32x16_bf16 v[48:63], v[72:75], v[100:103], v[48:63]
	ds_read_b64_tr_b16 v[72:73], v186 offset:0x1c00
	ds_read_b64_tr_b16 v[74:75], v186 offset:0x2400
	ds_read_b64_tr_b16 v[76:77], v186 offset:0x2c00
	ds_read_b64_tr_b16 v[218:219], v186 offset:0x3400
	ds_read_b64_tr_b16 v[220:221], v186 offset:0x3c00
	s_waitcnt lgkmcnt(0)
	v_mfma_f32_32x32x16_bf16 v[48:63], v[214:217], v[104:107], v[48:63]
	v_max_f32_e32 v64, v64, v65
	v_mfma_f32_32x32x16_bf16 v[16:31], v[66:69], v[96:99], v[16:31]
	v_cmp_ge_f32_e32 vcc, s25, v64
	s_cmp_eq_u64 vcc, exec
	v_mfma_f32_32x32x16_bf16 v[16:31], v[70:73], v[108:111], v[16:31]
	v_mfma_f32_32x32x16_bf16 v[16:31], v[74:77], v[100:103], v[16:31]
	v_mfma_f32_32x32x16_bf16 v[16:31], v[218:221], v[104:107], v[16:31]
	s_cbranch_scc0 .LBB4_737
	v_mov_b32_e32 v180, 1.0
.LBB4_706:
	ds_read_b64_tr_b16 v[214:215], v186 offset:0x600
	ds_read_b64_tr_b16 v[216:217], v186 offset:0xe00
	ds_read_b64_tr_b16 v[218:219], v186 offset:0x1600
	ds_read_b64_tr_b16 v[220:221], v186 offset:0x1e00
	ds_read_b64_tr_b16 v[222:223], v186 offset:0x2600
	ds_read_b64_tr_b16 v[224:225], v186 offset:0x2e00
	ds_read_b64_tr_b16 v[226:227], v186 offset:0x3600
	ds_read_b64_tr_b16 v[228:229], v186 offset:0x3e00
	s_waitcnt lgkmcnt(0)
	s_nop 0
	v_mfma_f32_32x32x16_bf16 v[0:15], v[214:217], v[96:99], v[0:15]
	v_exp_f32_e32 v186, v128
	v_exp_f32_e32 v230, v129
	v_exp_f32_e32 v231, v130
	v_exp_f32_e32 v232, v131
	s_lshl_b32 s2, s64, 14
	s_add_i32 s2, s2, 0
	s_lshl_b32 s3, s64, 13
	v_add_u32_e32 v96, s2, v200
	s_sub_i32 s78, s2, s3
	s_waitcnt vmcnt(0)
	v_add_u32_e32 v97, s2, v201
	v_mfma_f32_32x32x16_bf16 v[0:15], v[218:221], v[108:111], v[0:15]
	v_exp_f32_e32 v233, v132
	v_exp_f32_e32 v234, v133
	v_exp_f32_e32 v235, v134
	v_exp_f32_e32 v236, v135
	ds_write_b128 v96, v[176:179]
	v_add_u32_e32 v96, s78, v202
	ds_write_b128 v97, v[172:175]
	ds_write_b128 v96, v[168:171] offset:49152
	s_andn2_b64 s[2:3], exec, s[34:35]
	s_andn2_b64 vcc, exec, s[34:35]
	v_mfma_f32_32x32x16_bf16 v[0:15], v[222:225], v[100:103], v[0:15]
	v_exp_f32_e32 v237, v136
	v_exp_f32_e32 v238, v137
	v_exp_f32_e32 v239, v138
	v_exp_f32_e32 v240, v139
	v_mfma_f32_32x32x16_bf16 v[0:15], v[226:229], v[104:107], v[0:15]
	v_exp_f32_e32 v241, v140
	v_exp_f32_e32 v242, v141
	v_exp_f32_e32 v243, v142
	v_exp_f32_e32 v244, v143
	s_cbranch_vccnz .LBB4_711
	v_mul_f32_e32 v97, 0x44000000, v160
	v_mul_f32_e32 v98, 0x44000000, v164
	v_med3_f32 v97, v97, s62, v211
	v_med3_f32 v98, v98, s62, v211
	v_cvt_pk_fp8_f32 v99, v97, v98
	v_mul_f32_e32 v97, 0x44000000, v161
	v_mul_f32_e32 v98, 0x44000000, v165
	v_med3_f32 v97, v97, s62, v211
	v_med3_f32 v98, v98, s62, v211
	v_cvt_pk_fp8_f32 v100, v97, v98
	v_mul_f32_e32 v97, 0x44000000, v162
	v_mul_f32_e32 v98, 0x44000000, v166
	v_med3_f32 v97, v97, s62, v211
	v_med3_f32 v98, v98, s62, v211
	s_bitcmp1_b32 s58, 0
	v_cvt_pk_fp8_f32 v101, v97, v98
	v_mul_f32_e32 v97, 0x44000000, v163
	v_mul_f32_e32 v98, 0x44000000, v167
	s_cselect_b32 s8, 0x1100, 0
	v_med3_f32 v97, v97, s62, v211
	v_med3_f32 v98, v98, s62, v211
	v_cmp_eq_u32_e32 vcc, 0, v181
	v_add_u32_e32 v96, s8, v191
	v_cvt_pk_fp8_f32 v102, v97, v98
	s_and_b64 vcc, exec, vcc
	s_and_b32 s34, s58, 31
	ds_write_b16 v96, v99
	ds_write_b16 v96, v100 offset:68
	ds_write_b16 v96, v101 offset:136
	ds_write_b16 v96, v102 offset:204
	s_cbranch_vccnz .LBB4_735
	s_lshl_b32 s8, s34, 7
	s_lshl_b32 s9, s58, 6
	s_and_b32 s8, s8, 0xf00
	s_and_b32 s9, s9, 64
	s_or_b32 s26, s8, s9
	s_cbranch_execnz .LBB4_710

; DI void finishSM(f32x16& p0, f32x16& p1, float alpha, float& l_reg, bf16x8& pa0, bf16x8& pa1, bf16x8& pa2, bf16x8& pa3) {
; #pragma unroll
;     for (int r = 0; r < 16; ++r) p1[r] = __builtin_amdgcn_exp2f(p1[r]);
;     float ps = 0;
; #pragma unroll
;     for (int r = 0; r < 16; ++r) ps += p0[r];
; #pragma unroll
;     for (int r = 0; r < 16; ++r) ps += p1[r];
;     { auto rr = __builtin_amdgcn_permlane32_swap(__float_as_uint(ps), __float_as_uint(ps), false, false); ps = __uint_as_float(rr[0]) + __uint_as_float(rr[1]); }
;     l_reg = l_reg * alpha + ps;
;     ...
;     AT_PK4(p0, 0, pa0); AT_PK4(p0, 8, pa1); AT_PK4(p1, 0, pa2); AT_PK4(p1, 8, pa3);
;     ...
; }
; DI void qkt(f32x16& p0, f32x16& p1, const char* Ks, const bf16x8* qr, const f32x16& negm, int r32, int hi) {
; #pragma unroll
;     for (int d0 = 0; d0 < 4; ++d0) { const int cb = (d0 * 16 + hi * 8) * 2;
;         const bf16x8 b0 = *reinterpret_cast<const bf16x8*>(Ks + AT_KSWZ(r32, cb));
;         const bf16x8 b1 = *reinterpret_cast<const bf16x8*>(Ks + AT_KSWZ(32 + r32, cb));
;         p0 = __builtin_amdgcn_mfma_f32_32x32x16_bf16(b0, qr[d0], d0 == 0 ? negm : p0, 0, 0, 0);
;         p1 = __builtin_amdgcn_mfma_f32_32x32x16_bf16(b1, qr[d0], d0 == 0 ? negm : p1, 0, 0, 0); }
; DI void attn_pass(const Frame& F, CvRide& cv, const bf16_t* __restrict__ Qb, const bf16_t* __restrict__ Kh, const bf16_t* __restrict__ Vh, char* lds, f32x16 (&o)[4], float& l_out, const int wave_s) {
;     ...
;     const unsigned cv_ldo = (unsigned)(((tid >> 4) * 2 * 2048 + (tid & 15) * 4) * 4), cv_sto = (unsigned)((tid >> 3) * 2048 + 8 * (tid & 7));
;     const int cv_lw = OFF_CV + (4 * (tid & 15)) * 68 + 2 * (tid >> 4), cv_lr = OFF_CV + (tid >> 3) * 68 + 8 * (tid & 7);
;     f32x4 cvA = f32x4{}, cvB = f32x4{}; unsigned cvr0 = 0, cvr1 = 0;
.LBB4_723:
	v_add_u32_e32 v100, s78, v204
	ds_read_b128 v[96:99], v100 offset:49152
	ds_read_b128 v[168:171], v100 offset:53248
	v_add_u32_e32 v101, s78, v205
	v_add_u32_e32 v102, s78, v206
	v_add_u32_e32 v103, s78, v207
	ds_read_b128 v[172:175], v101 offset:49152
	ds_read_b128 v[176:179], v101 offset:53248
	ds_read_b128 v[214:217], v102 offset:49152
	ds_read_b128 v[218:221], v102 offset:53248
	ds_read_b128 v[222:225], v103 offset:49152
	ds_read_b128 v[226:229], v103 offset:53248
	v_exp_f32_e32 v112, v112
	v_exp_f32_e32 v113, v113
	v_exp_f32_e32 v114, v114
	s_waitcnt lgkmcnt(7)
	v_mfma_f32_32x32x16_bf16 v[128:143], v[96:99], v[156:159], v[80:95]
	v_exp_f32_e32 v115, v115
	v_exp_f32_e32 v116, v116
	v_exp_f32_e32 v117, v117
	v_exp_f32_e32 v118, v118
	v_exp_f32_e32 v119, v119
	s_waitcnt lgkmcnt(6)
	v_mfma_f32_32x32x16_bf16 v[96:111], v[168:171], v[156:159], v[80:95]
	v_exp_f32_e32 v168, v120
	v_add_f32_e32 v120, 0, v186
	v_add_f32_e32 v120, v230, v120
	v_add_f32_e32 v120, v231, v120
	v_add_f32_e32 v120, v232, v120
	v_add_f32_e32 v120, v233, v120
	v_add_f32_e32 v120, v234, v120
	v_add_f32_e32 v120, v235, v120
	v_add_f32_e32 v120, v236, v120
	v_add_f32_e32 v120, v237, v120
	v_add_f32_e32 v120, v238, v120
	s_waitcnt lgkmcnt(5)
	v_mfma_f32_32x32x16_bf16 v[128:143], v[172:175], v[152:155], v[128:143]
	v_add_f32_e32 v120, v239, v120
	v_add_f32_e32 v120, v240, v120
	v_add_f32_e32 v120, v241, v120
	v_add_f32_e32 v120, v242, v120
	v_add_f32_e32 v120, v243, v120
	v_add_f32_e32 v120, v244, v120
	v_add_f32_e32 v120, v112, v120
	s_waitcnt lgkmcnt(4)
	v_mfma_f32_32x32x16_bf16 v[96:111], v[176:179], v[152:155], v[96:111]
	v_add_f32_e32 v120, v113, v120
	v_add_f32_e32 v120, v114, v120
	v_add_f32_e32 v120, v115, v120
	v_add_f32_e32 v120, v116, v120
	v_exp_f32_e32 v169, v121
	v_add_f32_e32 v120, v117, v120
	v_exp_f32_e32 v170, v122
	s_waitcnt lgkmcnt(3)
	v_mfma_f32_32x32x16_bf16 v[128:143], v[214:217], v[148:151], v[128:143]
	v_add_f32_e32 v120, v118, v120
	v_exp_f32_e32 v171, v123
	v_add_f32_e32 v120, v119, v120
	v_exp_f32_e32 v172, v124
	v_add_f32_e32 v120, v168, v120
	v_exp_f32_e32 v173, v125
	v_add_f32_e32 v120, v169, v120
	s_waitcnt lgkmcnt(2)
	v_mfma_f32_32x32x16_bf16 v[96:111], v[218:221], v[148:151], v[96:111]
	v_exp_f32_e32 v174, v126
	v_add_f32_e32 v120, v170, v120
	v_exp_f32_e32 v175, v127
	v_add_f32_e32 v120, v171, v120
	v_add_f32_e32 v120, v172, v120
	v_add_f32_e32 v120, v173, v120
	v_add_f32_e32 v120, v174, v120
	s_waitcnt lgkmcnt(1)
	v_mfma_f32_32x32x16_bf16 v[128:143], v[222:225], v[144:147], v[128:143]
	v_add_f32_e32 v213, v175, v120
	v_mov_b32_e32 v214, v213
	v_cvt_pk_bf16_f32 v120, v186, v230
	v_cvt_pk_bf16_f32 v121, v231, v232
	v_cvt_pk_bf16_f32 v122, v233, v234
	v_cvt_pk_bf16_f32 v123, v235, v236
	v_cvt_pk_bf16_f32 v124, v237, v238
	s_waitcnt lgkmcnt(0)
	v_mfma_f32_32x32x16_bf16 v[96:111], v[226:229], v[144:147], v[96:111]
	v_cvt_pk_bf16_f32 v125, v239, v240
	v_cvt_pk_bf16_f32 v126, v241, v242
	v_cvt_pk_bf16_f32 v127, v243, v244
	v_cvt_pk_bf16_f32 v112, v112, v113
	v_cvt_pk_bf16_f32 v113, v114, v115
	v_cvt_pk_bf16_f32 v114, v116, v117
	v_cvt_pk_bf16_f32 v115, v118, v119
	v_cvt_pk_bf16_f32 v116, v168, v169
	v_cvt_pk_bf16_f32 v117, v170, v171
	v_cvt_pk_bf16_f32 v118, v172, v173
	v_cvt_pk_bf16_f32 v119, v174, v175
	v_permlane32_swap_b32_e32 v213, v214
	v_permlane32_swap_b32_e32 v120, v122
	v_permlane32_swap_b32_e32 v121, v123
	v_permlane32_swap_b32_e32 v124, v126
	v_permlane32_swap_b32_e32 v125, v127
	v_permlane32_swap_b32_e32 v112, v114
	v_permlane32_swap_b32_e32 v113, v115
	v_permlane32_swap_b32_e32 v116, v118
	v_permlane32_swap_b32_e32 v117, v119
	s_add_u32 s78, s74, 0x2380c000
	s_addc_u32 s79, s75, 0
	s_add_u32 s74, s74, 0x2380e000
	s_addc_u32 s75, s75, 0
	s_add_u32 s76, s76, 0x21806000
	s_addc_u32 s77, s77, 0
	v_mov_b32_e32 v168, v198
	v_mov_b32_e32 v169, v197
	global_load_dwordx4 v[176:179], v169, s[78:79]
	global_load_dwordx4 v[172:175], v169, s[74:75]
	s_nop 0
	global_load_dwordx4 v[168:171], v168, s[76:77]
	s_and_b64 vcc, exec, s[2:3]
	s_cbranch_vccnz .LBB4_725
	s_mov_b64 s[2:3], s[8:9]
	v_mov_b32_e32 v186, v189
	global_store_dwordx2 v186, v[184:185], s[2:3] nt
; DI void pv_all_sm(f32x16* o, int vb, bf16x8 pa0, bf16x8 pa1, bf16x8 pa2, bf16x8 pa3, f32x16& p0, f32x16& p1, float& m_ref, f32x16& negm, float& alpha) {
;     pv_one<0>(o[0], vb, pa0, pa1, pa2, pa3);
;     float pmax = p0[0];
; #pragma unroll
;     for (int r = 1; r < 16; ++r) pmax = fmaxf(pmax, p0[r]);
;     pv_one<1>(o[1], vb, pa0, pa1, pa2, pa3);
; #pragma unroll
;     for (int r = 0; r < 16; ++r) pmax = fmaxf(pmax, p1[r]);
;     { auto rr = __builtin_amdgcn_permlane32_swap(__float_as_uint(pmax), __float_as_uint(pmax), false, false); pmax = fmaxf(__uint_as_float(rr[0]), __uint_as_float(rr[1])); }
;     pv_one<2>(o[2], vb, pa0, pa1, pa2, pa3);
;     alpha = 1.f;
;     if (__builtin_expect(!__all(pmax <= THRL), 0)) {
;         const float dl = fmaxf(pmax, 0.f); m_ref += dl; alpha = __builtin_amdgcn_exp2f(-dl);
; #pragma unroll
;         for (int r = 0; r < 16; ++r) { p0[r] -= dl; p1[r] -= dl; }
; #pragma unroll
;         for (int r = 0; r < 16; ++r) negm[r] = -m_ref;
;     }
;     pv_one<3>(o[3], vb, pa0, pa1, pa2, pa3);
; #pragma unroll
;     for (int r = 0; r < 16; ++r) p0[r] = __builtin_amdgcn_exp2f(p0[r]);
; }
.LBB4_725:
	v_lshl_add_u32 v215, s66, 14, v192
	ds_read_b64_tr_b16 v[216:217], v215 offset:0
	ds_read_b64_tr_b16 v[218:219], v215 offset:0x800
	ds_read_b64_tr_b16 v[220:221], v215 offset:0x1000
	ds_read_b64_tr_b16 v[222:223], v215 offset:0x1800
	ds_read_b64_tr_b16 v[224:225], v215 offset:0x2000
	ds_read_b64_tr_b16 v[226:227], v215 offset:0x2800
	ds_read_b64_tr_b16 v[228:229], v215 offset:0x3000
	ds_read_b64_tr_b16 v[230:231], v215 offset:0x3800
	s_waitcnt lgkmcnt(0)
	s_nop 0
	v_mfma_f32_32x32x16_bf16 v[32:47], v[216:219], v[120:123], v[32:47]
	v_max_f32_e32 v186, v128, v129
	ds_read_b64_tr_b16 v[216:217], v215 offset:0x200
	ds_read_b64_tr_b16 v[218:219], v215 offset:0xa00
	v_max3_f32 v186, v186, v130, v131
	v_max3_f32 v186, v186, v132, v133
	v_mfma_f32_32x32x16_bf16 v[32:47], v[220:223], v[124:127], v[32:47]
	ds_read_b64_tr_b16 v[220:221], v215 offset:0x1200
	ds_read_b64_tr_b16 v[222:223], v215 offset:0x1a00
	v_max3_f32 v186, v186, v134, v135
	v_max3_f32 v186, v186, v136, v137
	v_max3_f32 v186, v186, v138, v139
	v_max3_f32 v186, v186, v140, v141
	v_max3_f32 v186, v186, v142, v143
	v_mfma_f32_32x32x16_bf16 v[32:47], v[224:227], v[112:115], v[32:47]
	ds_read_b64_tr_b16 v[224:225], v215 offset:0x2200
	ds_read_b64_tr_b16 v[226:227], v215 offset:0x2a00
	ds_read_b64_tr_b16 v[232:233], v215 offset:0x3200
	ds_read_b64_tr_b16 v[234:235], v215 offset:0x3a00
	s_waitcnt lgkmcnt(0)
	v_mfma_f32_32x32x16_bf16 v[32:47], v[228:231], v[116:119], v[32:47]
	v_mfma_f32_32x32x16_bf16 v[48:63], v[216:219], v[120:123], v[48:63]
	v_max3_f32 v186, v186, v96, v97
	v_max3_f32 v186, v186, v98, v99
	ds_read_b64_tr_b16 v[218:219], v215 offset:0x400
	v_max3_f32 v186, v186, v100, v101
	v_max3_f32 v186, v186, v102, v103
	v_max3_f32 v186, v186, v104, v105
	v_max3_f32 v186, v186, v106, v107
	v_mfma_f32_32x32x16_bf16 v[48:63], v[220:223], v[124:127], v[48:63]
	ds_read_b64_tr_b16 v[220:221], v215 offset:0xc00
	ds_read_b64_tr_b16 v[222:223], v215 offset:0x1400
	v_max3_f32 v186, v186, v108, v109
	v_max3_f32 v186, v186, v110, v111
	v_mov_b32_e32 v216, v186
	s_nop 1
	v_permlane32_swap_b32_e32 v186, v216
	v_mfma_f32_32x32x16_bf16 v[48:63], v[224:227], v[112:115], v[48:63]
	ds_read_b64_tr_b16 v[224:225], v215 offset:0x1c00
	ds_read_b64_tr_b16 v[226:227], v215 offset:0x2400
	ds_read_b64_tr_b16 v[228:229], v215 offset:0x2c00
	ds_read_b64_tr_b16 v[236:237], v215 offset:0x3400
	ds_read_b64_tr_b16 v[238:239], v215 offset:0x3c00
	s_waitcnt lgkmcnt(0)
	v_mfma_f32_32x32x16_bf16 v[48:63], v[232:235], v[116:119], v[48:63]
	v_max_f32_e32 v216, v186, v216
	v_mfma_f32_32x32x16_bf16 v[16:31], v[218:221], v[120:123], v[16:31]
	v_cmp_ge_f32_e32 vcc, s25, v216
	s_cmp_eq_u64 vcc, exec
	v_mov_b32_e32 v186, 1.0
	v_mfma_f32_32x32x16_bf16 v[16:31], v[222:225], v[124:127], v[16:31]
	v_mfma_f32_32x32x16_bf16 v[16:31], v[226:229], v[112:115], v[16:31]
	v_mfma_f32_32x32x16_bf16 v[16:31], v[236:239], v[116:119], v[16:31]
	s_cbranch_scc0 .LBB4_738
.LBB4_726:
	ds_read_b64_tr_b16 v[216:217], v215 offset:0x600
	ds_read_b64_tr_b16 v[218:219], v215 offset:0xe00
	ds_read_b64_tr_b16 v[220:221], v215 offset:0x1600
	ds_read_b64_tr_b16 v[222:223], v215 offset:0x1e00
	ds_read_b64_tr_b16 v[224:225], v215 offset:0x2600
	ds_read_b64_tr_b16 v[226:227], v215 offset:0x2e00
	ds_read_b64_tr_b16 v[228:229], v215 offset:0x3600
	ds_read_b64_tr_b16 v[230:231], v215 offset:0x3e00
	s_waitcnt lgkmcnt(0)
	s_nop 0
	v_mfma_f32_32x32x16_bf16 v[0:15], v[216:219], v[120:123], v[0:15]
	s_add_i32 s2, s67, 0
	v_add_u32_e32 v120, s2, v200
	s_waitcnt vmcnt(0)
	ds_write_b128 v120, v[176:179]
	s_mov_b32 s26, 0
	s_andn2_b64 vcc, exec, s[34:35]
	v_mfma_f32_32x32x16_bf16 v[0:15], v[220:223], v[124:127], v[0:15]
	v_mfma_f32_32x32x16_bf16 v[0:15], v[224:227], v[112:115], v[0:15]
	v_add_u32_e32 v112, s2, v201
	ds_write_b128 v112, v[172:175]
	v_lshl_add_u32 v112, s65, 13, v203
	ds_write_b128 v112, v[168:171] offset:49152
	s_andn2_b64 s[2:3], exec, s[34:35]
	v_mfma_f32_32x32x16_bf16 v[0:15], v[228:231], v[116:119], v[0:15]
	s_cbranch_vccnz .LBB4_731
	v_mul_f32_e32 v113, 0x44000000, v160
	v_mul_f32_e32 v114, 0x44000000, v164
	v_med3_f32 v113, v113, s62, v211
	v_med3_f32 v114, v114, s62, v211
	v_cvt_pk_fp8_f32 v115, v113, v114
	v_mul_f32_e32 v113, 0x44000000, v161
	v_mul_f32_e32 v114, 0x44000000, v165
	v_med3_f32 v113, v113, s62, v211
	v_med3_f32 v114, v114, s62, v211
	v_cvt_pk_fp8_f32 v116, v113, v114
	v_mul_f32_e32 v113, 0x44000000, v162
	v_mul_f32_e32 v114, 0x44000000, v166
	v_med3_f32 v113, v113, s62, v211
	v_med3_f32 v114, v114, s62, v211
	s_bitcmp1_b32 s58, 0
	v_cvt_pk_fp8_f32 v117, v113, v114
	v_mul_f32_e32 v113, 0x44000000, v163
	v_mul_f32_e32 v114, 0x44000000, v167
	s_cselect_b32 s8, 0x1100, 0
	v_med3_f32 v113, v113, s62, v211
	v_med3_f32 v114, v114, s62, v211
	v_cmp_eq_u32_e32 vcc, 0, v181
	v_add_u32_e32 v112, s8, v191
	v_cvt_pk_fp8_f32 v118, v113, v114
	s_and_b64 vcc, exec, vcc
	s_and_b32 s37, s58, 31
	ds_write_b16 v112, v115
	ds_write_b16 v112, v116 offset:68
	ds_write_b16 v112, v117 offset:136
	ds_write_b16 v112, v118 offset:204
	s_cbranch_vccnz .LBB4_736
	s_lshl_b32 s8, s37, 7
	s_lshl_b32 s9, s58, 6
	s_and_b32 s8, s8, 0xf00
	s_and_b32 s9, s9, 64
	s_or_b32 s26, s8, s9
	s_cbranch_execnz .LBB4_730

; #define AT_SBAR() __builtin_amdgcn_sched_barrier(0)
; #define AT_CV_READ() do { if (cv.pend) { const char* t_ = lds + cv_lr + ((cv.ci - 1) & 1) * CV_TILE; cvr0 = *(const unsigned*)t_; cvr1 = *(const unsigned*)(t_ + 4); } } while (0)
; #define AT_CV_STORE() do { if (cv.pend) { GAS unsigned char* gd_ = (GAS unsigned char*)cv.sdst; unsigned o_ = cv_sto; asm volatile("" : "+s"(gd_), "+v"(o_)); __builtin_nontemporal_store((u32x2){cvr0, cvr1}, (GAS u32x2*)(gd_ + (size_t)o_)); cv.pend = 0; } } while (0)
; DI void attn_pass(const Frame& F, CvRide& cv, const bf16_t* __restrict__ Qb, const bf16_t* __restrict__ Kh, const bf16_t* __restrict__ Vh, char* lds, f32x16 (&o)[4], float& l_out, const int wave_s) {
;     ...
;     for (int j = 1; j + 2 < NT; j += 2) {
;         AT_STEP(pB0, pB1, pA0, pA1, alB, alA, j, true);
;         AT_STEP(pA0, pA1, pB0, pB1, alA, alB, j + 1, true);
;     }
;     AT_STEP(pB0, pB1, pA0, pA1, alB, alA, NT - 1, false);
;     AT_CV_READ(); AT_CV_STORE();
;     finishSM(pB0, pB1, alB, l_reg, pa0, pa1, pa2, pa3); AT_SBAR();
;     pv_all(o, vb0 + s_prev * SHM_V, pa0, pa1, pa2, pa3);
.LBB4_739:
	v_mov_b64_e32 v[64:65], v[80:81]
	v_mov_b64_e32 v[66:67], v[82:83]
	v_mov_b64_e32 v[68:69], v[84:85]
	v_mov_b64_e32 v[70:71], v[86:87]
	v_mov_b64_e32 v[72:73], v[88:89]
	v_mov_b64_e32 v[74:75], v[90:91]
	v_mov_b64_e32 v[76:77], v[92:93]
	v_mov_b64_e32 v[78:79], v[94:95]
	s_and_b64 vcc, exec, s[34:35]
	s_cbranch_vccz .LBB4_741
	s_andn2_b32 s15, 1, s58
	s_mulk_i32 s15, 0x1100
	v_add_u32_e32 v80, s15, v190
	ds_read2_b32 v[184:185], v80 offset1:1

; DI void pv_all_sm(f32x16* o, int vb, bf16x8 pa0, bf16x8 pa1, bf16x8 pa2, bf16x8 pa3, f32x16& p0, f32x16& p1, float& m_ref, f32x16& negm, float& alpha) {
;     pv_one<0>(o[0], vb, pa0, pa1, pa2, pa3);
;     float pmax = p0[0];
; #pragma unroll
;     for (int r = 1; r < 16; ++r) pmax = fmaxf(pmax, p0[r]);
;     pv_one<1>(o[1], vb, pa0, pa1, pa2, pa3);
; #pragma unroll
;     for (int r = 0; r < 16; ++r) pmax = fmaxf(pmax, p1[r]);
;     { auto rr = __builtin_amdgcn_permlane32_swap(__float_as_uint(pmax), __float_as_uint(pmax), false, false); pmax = fmaxf(__uint_as_float(rr[0]), __uint_as_float(rr[1])); }
;     pv_one<2>(o[2], vb, pa0, pa1, pa2, pa3);
;     alpha = 1.f;
;     if (__builtin_expect(!__all(pmax <= THRL), 0)) {
;         const float dl = fmaxf(pmax, 0.f); m_ref += dl; alpha = __builtin_amdgcn_exp2f(-dl);
; #pragma unroll
;         for (int r = 0; r < 16; ++r) { p0[r] -= dl; p1[r] -= dl; }
; #pragma unroll
;         for (int r = 0; r < 16; ++r) negm[r] = -m_ref;
;     }
;     pv_one<3>(o[3], vb, pa0, pa1, pa2, pa3);
; #pragma unroll
;     for (int r = 0; r < 16; ++r) p0[r] = __builtin_amdgcn_exp2f(p0[r]);
; }
.LBB4_777:
	s_lshl_b32 s31, s29, 14
	v_add_u32_e32 v182, s31, v192
	ds_read_b64_tr_b16 v[64:65], v182 offset:0
	ds_read_b64_tr_b16 v[66:67], v182 offset:0x800
	ds_read_b64_tr_b16 v[68:69], v182 offset:0x1000
	ds_read_b64_tr_b16 v[70:71], v182 offset:0x1800
	ds_read_b64_tr_b16 v[72:73], v182 offset:0x2000
	ds_read_b64_tr_b16 v[74:75], v182 offset:0x2800
	ds_read_b64_tr_b16 v[76:77], v182 offset:0x3000
	ds_read_b64_tr_b16 v[78:79], v182 offset:0x3800
	s_waitcnt lgkmcnt(0)
	s_nop 0
	v_mfma_f32_32x32x16_bf16 v[48:63], v[64:67], v[96:99], v[48:63]
	v_max_f32_e32 v64, v128, v129
	v_max3_f32 v64, v64, v130, v131
	v_max3_f32 v64, v64, v132, v133
	v_max3_f32 v64, v64, v134, v135
	v_max3_f32 v64, v64, v136, v137
	v_mfma_f32_32x32x16_bf16 v[48:63], v[68:71], v[108:111], v[48:63]
	v_max3_f32 v64, v64, v138, v139
	v_max3_f32 v66, v64, v140, v141
	ds_read_b64_tr_b16 v[64:65], v182 offset:0x200
	v_max3_f32 v180, v66, v142, v143
	ds_read_b64_tr_b16 v[66:67], v182 offset:0xa00
	ds_read_b64_tr_b16 v[68:69], v182 offset:0x1200
	ds_read_b64_tr_b16 v[70:71], v182 offset:0x1a00
	v_mfma_f32_32x32x16_bf16 v[48:63], v[72:75], v[100:103], v[48:63]
	ds_read_b64_tr_b16 v[72:73], v182 offset:0x2200
	ds_read_b64_tr_b16 v[74:75], v182 offset:0x2a00
	ds_read_b64_tr_b16 v[218:219], v182 offset:0x3200
	ds_read_b64_tr_b16 v[220:221], v182 offset:0x3a00
	s_waitcnt lgkmcnt(0)
	v_mfma_f32_32x32x16_bf16 v[48:63], v[76:79], v[104:107], v[48:63]
	v_mfma_f32_32x32x16_bf16 v[32:47], v[64:67], v[96:99], v[32:47]
	v_max3_f32 v76, v180, v112, v113
	v_max3_f32 v64, v76, v114, v115
	ds_read_b64_tr_b16 v[66:67], v182 offset:0x400
	v_max3_f32 v64, v64, v116, v117
	v_max3_f32 v64, v64, v118, v119
	v_max3_f32 v64, v64, v120, v121
	v_max3_f32 v64, v64, v122, v123
	v_mfma_f32_32x32x16_bf16 v[32:47], v[68:71], v[108:111], v[32:47]
	ds_read_b64_tr_b16 v[68:69], v182 offset:0xc00
	ds_read_b64_tr_b16 v[70:71], v182 offset:0x1400
	v_max3_f32 v64, v64, v124, v125
	v_max3_f32 v64, v64, v126, v127
	v_mov_b32_e32 v65, v64
	s_nop 1
	v_permlane32_swap_b32_e32 v64, v65
	v_mfma_f32_32x32x16_bf16 v[32:47], v[72:75], v[100:103], v[32:47]
	ds_read_b64_tr_b16 v[72:73], v182 offset:0x1c00
	ds_read_b64_tr_b16 v[74:75], v182 offset:0x2400
	ds_read_b64_tr_b16 v[76:77], v182 offset:0x2c00
	ds_read_b64_tr_b16 v[222:223], v182 offset:0x3400
	ds_read_b64_tr_b16 v[224:225], v182 offset:0x3c00
	s_waitcnt lgkmcnt(0)
	v_mfma_f32_32x32x16_bf16 v[32:47], v[218:221], v[104:107], v[32:47]
	v_max_f32_e32 v64, v64, v65
	v_mfma_f32_32x32x16_bf16 v[16:31], v[66:69], v[96:99], v[16:31]
	v_cmp_ge_f32_e32 vcc, s26, v64
	s_cmp_eq_u64 vcc, exec
	v_mfma_f32_32x32x16_bf16 v[16:31], v[70:73], v[108:111], v[16:31]
	v_mfma_f32_32x32x16_bf16 v[16:31], v[74:77], v[100:103], v[16:31]
	v_mfma_f32_32x32x16_bf16 v[16:31], v[222:225], v[104:107], v[16:31]
	s_cbranch_scc0 .LBB4_810
	v_mov_b32_e32 v180, 1.0
.LBB4_779:
	ds_read_b64_tr_b16 v[218:219], v182 offset:0x600
	ds_read_b64_tr_b16 v[220:221], v182 offset:0xe00
	ds_read_b64_tr_b16 v[222:223], v182 offset:0x1600
	ds_read_b64_tr_b16 v[224:225], v182 offset:0x1e00
	ds_read_b64_tr_b16 v[226:227], v182 offset:0x2600
	ds_read_b64_tr_b16 v[228:229], v182 offset:0x2e00
	ds_read_b64_tr_b16 v[230:231], v182 offset:0x3600
	ds_read_b64_tr_b16 v[232:233], v182 offset:0x3e00
	s_waitcnt lgkmcnt(0)
	s_nop 0
	v_mfma_f32_32x32x16_bf16 v[0:15], v[218:221], v[96:99], v[0:15]
	v_exp_f32_e32 v182, v128
	v_exp_f32_e32 v234, v129
	v_exp_f32_e32 v235, v130
	v_exp_f32_e32 v236, v131
	s_lshl_b32 s2, s15, 14
	s_add_i32 s2, s2, 0
	s_lshl_b32 s3, s15, 13
	v_add_u32_e32 v96, s2, v203
	s_sub_i32 s65, s2, s3
	s_waitcnt vmcnt(0)
	v_add_u32_e32 v97, s2, v204
	v_mfma_f32_32x32x16_bf16 v[0:15], v[222:225], v[108:111], v[0:15]
	v_exp_f32_e32 v237, v132
	v_exp_f32_e32 v238, v133
	v_exp_f32_e32 v239, v134
	v_exp_f32_e32 v240, v135
	ds_write_b128 v96, v[176:179]
	v_add_u32_e32 v96, s65, v205
	ds_write_b128 v97, v[172:175]
	ds_write_b128 v96, v[168:171] offset:49152
	s_andn2_b64 s[2:3], exec, s[22:23]
	s_andn2_b64 vcc, exec, s[22:23]
	v_mfma_f32_32x32x16_bf16 v[0:15], v[226:229], v[100:103], v[0:15]
	v_exp_f32_e32 v241, v136
	v_exp_f32_e32 v242, v137
	v_exp_f32_e32 v243, v138
	v_exp_f32_e32 v244, v139
	v_mfma_f32_32x32x16_bf16 v[0:15], v[230:233], v[104:107], v[0:15]
	v_exp_f32_e32 v245, v140
	v_exp_f32_e32 v246, v141
	v_exp_f32_e32 v247, v142
	v_exp_f32_e32 v248, v143
	s_cbranch_vccnz .LBB4_784
	v_mul_f32_e32 v97, 0x44000000, v160
	v_mul_f32_e32 v98, 0x44000000, v164
	v_med3_f32 v97, v97, s28, v214
	v_med3_f32 v98, v98, s28, v214
	v_cvt_pk_fp8_f32 v99, v97, v98
	v_mul_f32_e32 v97, 0x44000000, v161
	v_mul_f32_e32 v98, 0x44000000, v165
	v_med3_f32 v97, v97, s28, v214
	v_med3_f32 v98, v98, s28, v214
	v_cvt_pk_fp8_f32 v100, v97, v98
	v_mul_f32_e32 v97, 0x44000000, v162
	v_mul_f32_e32 v98, 0x44000000, v166
	v_med3_f32 v97, v97, s28, v214
	v_med3_f32 v98, v98, s28, v214
	s_bitcmp1_b32 s58, 0
	v_cvt_pk_fp8_f32 v101, v97, v98
	v_mul_f32_e32 v97, 0x44000000, v163
	v_mul_f32_e32 v98, 0x44000000, v167
	s_cselect_b32 s8, 0x1100, 0
	v_med3_f32 v97, v97, s28, v214
	v_med3_f32 v98, v98, s28, v214
	v_cmp_eq_u32_e32 vcc, 0, v181
	v_add_u32_e32 v96, s8, v195
	v_cvt_pk_fp8_f32 v102, v97, v98
	s_and_b64 vcc, exec, vcc
	s_and_b32 s22, s58, 31
	ds_write_b16 v96, v99
	ds_write_b16 v96, v100 offset:68
	ds_write_b16 v96, v101 offset:136
	ds_write_b16 v96, v102 offset:204
	s_cbranch_vccnz .LBB4_808
	s_lshl_b32 s8, s22, 7
	s_lshl_b32 s9, s58, 6
	s_and_b32 s8, s8, 0xf00
	s_and_b32 s9, s9, 64
	s_or_b32 s20, s8, s9
	s_cbranch_execnz .LBB4_783

; DI void finishSM(f32x16& p0, f32x16& p1, float alpha, float& l_reg, bf16x8& pa0, bf16x8& pa1, bf16x8& pa2, bf16x8& pa3) {
; #pragma unroll
;     for (int r = 0; r < 16; ++r) p1[r] = __builtin_amdgcn_exp2f(p1[r]);
;     float ps = 0;
; #pragma unroll
;     for (int r = 0; r < 16; ++r) ps += p0[r];
; #pragma unroll
;     for (int r = 0; r < 16; ++r) ps += p1[r];
;     { auto rr = __builtin_amdgcn_permlane32_swap(__float_as_uint(ps), __float_as_uint(ps), false, false); ps = __uint_as_float(rr[0]) + __uint_as_float(rr[1]); }
;     l_reg = l_reg * alpha + ps;
;     ...
;     AT_PK4(p0, 0, pa0); AT_PK4(p0, 8, pa1); AT_PK4(p1, 0, pa2); AT_PK4(p1, 8, pa3);
;     ...
; }
; DI void qkt(f32x16& p0, f32x16& p1, const char* Ks, const bf16x8* qr, const f32x16& negm, int r32, int hi) {
; #pragma unroll
;     for (int d0 = 0; d0 < 4; ++d0) { const int cb = (d0 * 16 + hi * 8) * 2;
;         const bf16x8 b0 = *reinterpret_cast<const bf16x8*>(Ks + AT_KSWZ(r32, cb));
;         const bf16x8 b1 = *reinterpret_cast<const bf16x8*>(Ks + AT_KSWZ(32 + r32, cb));
;         p0 = __builtin_amdgcn_mfma_f32_32x32x16_bf16(b0, qr[d0], d0 == 0 ? negm : p0, 0, 0, 0);
;         p1 = __builtin_amdgcn_mfma_f32_32x32x16_bf16(b1, qr[d0], d0 == 0 ? negm : p1, 0, 0, 0); }
; DI void attn_pass(const Frame& F, CvRide& cv, const bf16_t* __restrict__ Qb, const bf16_t* __restrict__ Kh, const bf16_t* __restrict__ Vh, char* lds, f32x16 (&o)[4], float& l_out, const int wave_s) {
;     ...
;     const unsigned cv_ldo = (unsigned)(((tid >> 4) * 2 * 2048 + (tid & 15) * 4) * 4), cv_sto = (unsigned)((tid >> 3) * 2048 + 8 * (tid & 7));
;     const int cv_lw = OFF_CV + (4 * (tid & 15)) * 68 + 2 * (tid >> 4), cv_lr = OFF_CV + (tid >> 3) * 68 + 8 * (tid & 7);
;     f32x4 cvA = f32x4{}, cvB = f32x4{}; unsigned cvr0 = 0, cvr1 = 0;
.LBB4_796:
	v_add_u32_e32 v100, s65, v207
	ds_read_b128 v[96:99], v100 offset:49152
	ds_read_b128 v[168:171], v100 offset:53248
	v_add_u32_e32 v101, s65, v208
	v_add_u32_e32 v102, s65, v209
	v_add_u32_e32 v103, s65, v210
	ds_read_b128 v[172:175], v101 offset:49152
	ds_read_b128 v[176:179], v101 offset:53248
	ds_read_b128 v[218:221], v102 offset:49152
	ds_read_b128 v[222:225], v102 offset:53248
	ds_read_b128 v[226:229], v103 offset:49152
	ds_read_b128 v[230:233], v103 offset:53248
	v_exp_f32_e32 v112, v112
	v_exp_f32_e32 v113, v113
	v_exp_f32_e32 v114, v114
	s_waitcnt lgkmcnt(7)
	v_mfma_f32_32x32x16_bf16 v[128:143], v[96:99], v[156:159], v[80:95]
	v_exp_f32_e32 v115, v115
	v_exp_f32_e32 v116, v116
	v_exp_f32_e32 v117, v117
	v_exp_f32_e32 v118, v118
	v_exp_f32_e32 v119, v119
	s_waitcnt lgkmcnt(6)
	v_mfma_f32_32x32x16_bf16 v[96:111], v[168:171], v[156:159], v[80:95]
	v_exp_f32_e32 v168, v120
	v_add_f32_e32 v120, 0, v182
	v_add_f32_e32 v120, v234, v120
	v_add_f32_e32 v120, v235, v120
	v_add_f32_e32 v120, v236, v120
	v_add_f32_e32 v120, v237, v120
	v_add_f32_e32 v120, v238, v120
	v_add_f32_e32 v120, v239, v120
	v_add_f32_e32 v120, v240, v120
	v_add_f32_e32 v120, v241, v120
	v_add_f32_e32 v120, v242, v120
	s_waitcnt lgkmcnt(5)
	v_mfma_f32_32x32x16_bf16 v[128:143], v[172:175], v[152:155], v[128:143]
	v_add_f32_e32 v120, v243, v120
	v_add_f32_e32 v120, v244, v120
	v_add_f32_e32 v120, v245, v120
	v_add_f32_e32 v120, v246, v120
	v_add_f32_e32 v120, v247, v120
	v_add_f32_e32 v120, v248, v120
	v_add_f32_e32 v120, v112, v120
	s_waitcnt lgkmcnt(4)
	v_mfma_f32_32x32x16_bf16 v[96:111], v[176:179], v[152:155], v[96:111]
	v_add_f32_e32 v120, v113, v120
	v_add_f32_e32 v120, v114, v120
	v_add_f32_e32 v120, v115, v120
	v_add_f32_e32 v120, v116, v120
	v_exp_f32_e32 v169, v121
	v_add_f32_e32 v120, v117, v120
	v_exp_f32_e32 v170, v122
	s_waitcnt lgkmcnt(3)
	v_mfma_f32_32x32x16_bf16 v[128:143], v[218:221], v[148:151], v[128:143]
	v_add_f32_e32 v120, v118, v120
	v_exp_f32_e32 v171, v123
	v_add_f32_e32 v120, v119, v120
	v_exp_f32_e32 v172, v124
	v_add_f32_e32 v120, v168, v120
	v_exp_f32_e32 v173, v125
	v_add_f32_e32 v120, v169, v120
	s_waitcnt lgkmcnt(2)
	v_mfma_f32_32x32x16_bf16 v[96:111], v[222:225], v[148:151], v[96:111]
	v_exp_f32_e32 v174, v126
	v_add_f32_e32 v120, v170, v120
	v_exp_f32_e32 v175, v127
	v_add_f32_e32 v120, v171, v120
	v_add_f32_e32 v120, v172, v120
	v_add_f32_e32 v120, v173, v120
	v_add_f32_e32 v120, v174, v120
	s_waitcnt lgkmcnt(1)
	v_mfma_f32_32x32x16_bf16 v[128:143], v[226:229], v[144:147], v[128:143]
	v_add_f32_e32 v217, v175, v120
	v_mov_b32_e32 v218, v217
	v_cvt_pk_bf16_f32 v120, v182, v234
	v_cvt_pk_bf16_f32 v121, v235, v236
	v_cvt_pk_bf16_f32 v122, v237, v238
	v_cvt_pk_bf16_f32 v123, v239, v240
	v_cvt_pk_bf16_f32 v124, v241, v242
	s_waitcnt lgkmcnt(0)
	v_mfma_f32_32x32x16_bf16 v[96:111], v[230:233], v[144:147], v[96:111]
	v_cvt_pk_bf16_f32 v125, v243, v244
	v_cvt_pk_bf16_f32 v126, v245, v246
	v_cvt_pk_bf16_f32 v127, v247, v248
	v_cvt_pk_bf16_f32 v112, v112, v113
	v_cvt_pk_bf16_f32 v113, v114, v115
	v_cvt_pk_bf16_f32 v114, v116, v117
	v_cvt_pk_bf16_f32 v115, v118, v119
	v_cvt_pk_bf16_f32 v116, v168, v169
	v_cvt_pk_bf16_f32 v117, v170, v171
	v_cvt_pk_bf16_f32 v118, v172, v173
	v_cvt_pk_bf16_f32 v119, v174, v175
	v_permlane32_swap_b32_e32 v217, v218
	v_permlane32_swap_b32_e32 v120, v122
	v_permlane32_swap_b32_e32 v121, v123
	v_permlane32_swap_b32_e32 v124, v126
	v_permlane32_swap_b32_e32 v125, v127
	v_permlane32_swap_b32_e32 v112, v114
	v_permlane32_swap_b32_e32 v113, v115
	v_permlane32_swap_b32_e32 v116, v118
	v_permlane32_swap_b32_e32 v117, v119
	s_add_u32 s24, s34, 0x2380c000
	s_addc_u32 s25, s35, 0
	s_add_u32 s34, s34, 0x2380e000
	s_addc_u32 s35, s35, 0
	s_add_u32 s66, s37, 0x21886000
	s_addc_u32 s67, s64, 0
	v_mov_b32_e32 v168, v200
	v_mov_b32_e32 v169, v201
	global_load_dwordx4 v[176:179], v168, s[24:25]
	global_load_dwordx4 v[172:175], v168, s[34:35]
	s_nop 0
	global_load_dwordx4 v[168:171], v169, s[66:67]
	s_and_b64 vcc, exec, s[2:3]
	s_cbranch_vccnz .LBB4_798
	v_mov_b32_e32 v182, v193
	s_mov_b64 s[2:3], s[8:9]
	global_store_dwordx2 v182, v[184:185], s[2:3] nt
; DI void pv_all_sm(f32x16* o, int vb, bf16x8 pa0, bf16x8 pa1, bf16x8 pa2, bf16x8 pa3, f32x16& p0, f32x16& p1, float& m_ref, f32x16& negm, float& alpha) {
;     pv_one<0>(o[0], vb, pa0, pa1, pa2, pa3);
;     float pmax = p0[0];
; #pragma unroll
;     for (int r = 1; r < 16; ++r) pmax = fmaxf(pmax, p0[r]);
;     pv_one<1>(o[1], vb, pa0, pa1, pa2, pa3);
; #pragma unroll
;     for (int r = 0; r < 16; ++r) pmax = fmaxf(pmax, p1[r]);
;     { auto rr = __builtin_amdgcn_permlane32_swap(__float_as_uint(pmax), __float_as_uint(pmax), false, false); pmax = fmaxf(__uint_as_float(rr[0]), __uint_as_float(rr[1])); }
;     pv_one<2>(o[2], vb, pa0, pa1, pa2, pa3);
;     alpha = 1.f;
;     if (__builtin_expect(!__all(pmax <= THRL), 0)) {
;         const float dl = fmaxf(pmax, 0.f); m_ref += dl; alpha = __builtin_amdgcn_exp2f(-dl);
; #pragma unroll
;         for (int r = 0; r < 16; ++r) { p0[r] -= dl; p1[r] -= dl; }
; #pragma unroll
;         for (int r = 0; r < 16; ++r) negm[r] = -m_ref;
;     }
;     pv_one<3>(o[3], vb, pa0, pa1, pa2, pa3);
; #pragma unroll
;     for (int r = 0; r < 16; ++r) p0[r] = __builtin_amdgcn_exp2f(p0[r]);
; }
.LBB4_798:
	v_lshl_add_u32 v219, s30, 14, v192
	ds_read_b64_tr_b16 v[220:221], v219 offset:0
	ds_read_b64_tr_b16 v[222:223], v219 offset:0x800
	ds_read_b64_tr_b16 v[224:225], v219 offset:0x1000
	ds_read_b64_tr_b16 v[226:227], v219 offset:0x1800
	ds_read_b64_tr_b16 v[228:229], v219 offset:0x2000
	ds_read_b64_tr_b16 v[230:231], v219 offset:0x2800
	ds_read_b64_tr_b16 v[232:233], v219 offset:0x3000
	ds_read_b64_tr_b16 v[234:235], v219 offset:0x3800
	s_waitcnt lgkmcnt(0)
	s_nop 0
	v_mfma_f32_32x32x16_bf16 v[48:63], v[220:223], v[120:123], v[48:63]
	v_max_f32_e32 v182, v128, v129
	ds_read_b64_tr_b16 v[220:221], v219 offset:0x200
	ds_read_b64_tr_b16 v[222:223], v219 offset:0xa00
	v_max3_f32 v182, v182, v130, v131
	v_max3_f32 v182, v182, v132, v133
	v_mfma_f32_32x32x16_bf16 v[48:63], v[224:227], v[124:127], v[48:63]
	ds_read_b64_tr_b16 v[224:225], v219 offset:0x1200
	ds_read_b64_tr_b16 v[226:227], v219 offset:0x1a00
	v_max3_f32 v182, v182, v134, v135
	v_max3_f32 v182, v182, v136, v137
	v_max3_f32 v182, v182, v138, v139
	v_max3_f32 v182, v182, v140, v141
	v_max3_f32 v182, v182, v142, v143
	v_mfma_f32_32x32x16_bf16 v[48:63], v[228:231], v[112:115], v[48:63]
	ds_read_b64_tr_b16 v[228:229], v219 offset:0x2200
	ds_read_b64_tr_b16 v[230:231], v219 offset:0x2a00
	ds_read_b64_tr_b16 v[236:237], v219 offset:0x3200
	ds_read_b64_tr_b16 v[238:239], v219 offset:0x3a00
	s_waitcnt lgkmcnt(0)
	v_mfma_f32_32x32x16_bf16 v[48:63], v[232:235], v[116:119], v[48:63]
	v_mfma_f32_32x32x16_bf16 v[32:47], v[220:223], v[120:123], v[32:47]
	v_max3_f32 v182, v182, v96, v97
	v_max3_f32 v182, v182, v98, v99
	ds_read_b64_tr_b16 v[222:223], v219 offset:0x400
	v_max3_f32 v182, v182, v100, v101
	v_max3_f32 v182, v182, v102, v103
	v_max3_f32 v182, v182, v104, v105
	v_max3_f32 v182, v182, v106, v107
	v_mfma_f32_32x32x16_bf16 v[32:47], v[224:227], v[124:127], v[32:47]
	ds_read_b64_tr_b16 v[224:225], v219 offset:0xc00
	ds_read_b64_tr_b16 v[226:227], v219 offset:0x1400
	v_max3_f32 v182, v182, v108, v109
	v_max3_f32 v182, v182, v110, v111
	v_mov_b32_e32 v220, v182
	s_nop 1
	v_permlane32_swap_b32_e32 v182, v220
	v_mfma_f32_32x32x16_bf16 v[32:47], v[228:231], v[112:115], v[32:47]
	ds_read_b64_tr_b16 v[228:229], v219 offset:0x1c00
	ds_read_b64_tr_b16 v[230:231], v219 offset:0x2400
	ds_read_b64_tr_b16 v[232:233], v219 offset:0x2c00
	ds_read_b64_tr_b16 v[240:241], v219 offset:0x3400
	ds_read_b64_tr_b16 v[242:243], v219 offset:0x3c00
	s_waitcnt lgkmcnt(0)
	v_mfma_f32_32x32x16_bf16 v[32:47], v[236:239], v[116:119], v[32:47]
	v_max_f32_e32 v220, v182, v220
	v_mfma_f32_32x32x16_bf16 v[16:31], v[222:225], v[120:123], v[16:31]
	v_cmp_ge_f32_e32 vcc, s26, v220
	s_cmp_eq_u64 vcc, exec
	v_mov_b32_e32 v182, 1.0
	v_mfma_f32_32x32x16_bf16 v[16:31], v[226:229], v[124:127], v[16:31]
	v_mfma_f32_32x32x16_bf16 v[16:31], v[230:233], v[112:115], v[16:31]
	v_mfma_f32_32x32x16_bf16 v[16:31], v[240:243], v[116:119], v[16:31]
	s_cbranch_scc0 .LBB4_811
.LBB4_799:
	ds_read_b64_tr_b16 v[220:221], v219 offset:0x600
	ds_read_b64_tr_b16 v[222:223], v219 offset:0xe00
	ds_read_b64_tr_b16 v[224:225], v219 offset:0x1600
	ds_read_b64_tr_b16 v[226:227], v219 offset:0x1e00
	ds_read_b64_tr_b16 v[228:229], v219 offset:0x2600
	ds_read_b64_tr_b16 v[230:231], v219 offset:0x2e00
	ds_read_b64_tr_b16 v[232:233], v219 offset:0x3600
	ds_read_b64_tr_b16 v[234:235], v219 offset:0x3e00
	s_waitcnt lgkmcnt(0)
	s_nop 0
	v_mfma_f32_32x32x16_bf16 v[0:15], v[220:223], v[120:123], v[0:15]
	s_add_i32 s2, s31, 0
	v_add_u32_e32 v120, s2, v203
	s_waitcnt vmcnt(0)
	ds_write_b128 v120, v[176:179]
	s_mov_b32 s20, 0
	s_andn2_b64 vcc, exec, s[22:23]
	v_mfma_f32_32x32x16_bf16 v[0:15], v[224:227], v[124:127], v[0:15]
	v_mfma_f32_32x32x16_bf16 v[0:15], v[228:231], v[112:115], v[0:15]
	v_add_u32_e32 v112, s2, v204
	ds_write_b128 v112, v[172:175]
	v_lshl_add_u32 v112, s29, 13, v206
	ds_write_b128 v112, v[168:171] offset:49152
	s_andn2_b64 s[2:3], exec, s[22:23]
	v_mfma_f32_32x32x16_bf16 v[0:15], v[232:235], v[116:119], v[0:15]
	s_cbranch_vccnz .LBB4_804
	v_mul_f32_e32 v113, 0x44000000, v160
	v_mul_f32_e32 v114, 0x44000000, v164
	v_med3_f32 v113, v113, s28, v214
	v_med3_f32 v114, v114, s28, v214
	v_cvt_pk_fp8_f32 v115, v113, v114
	v_mul_f32_e32 v113, 0x44000000, v161
	v_mul_f32_e32 v114, 0x44000000, v165
	v_med3_f32 v113, v113, s28, v214
	v_med3_f32 v114, v114, s28, v214
	v_cvt_pk_fp8_f32 v116, v113, v114
	v_mul_f32_e32 v113, 0x44000000, v162
	v_mul_f32_e32 v114, 0x44000000, v166
	v_med3_f32 v113, v113, s28, v214
	v_med3_f32 v114, v114, s28, v214
	s_bitcmp1_b32 s58, 0
	v_cvt_pk_fp8_f32 v117, v113, v114
	v_mul_f32_e32 v113, 0x44000000, v163
	v_mul_f32_e32 v114, 0x44000000, v167
	s_cselect_b32 s8, 0x1100, 0
	v_med3_f32 v113, v113, s28, v214
	v_med3_f32 v114, v114, s28, v214
	v_cmp_eq_u32_e32 vcc, 0, v181
	v_add_u32_e32 v112, s8, v195
	v_cvt_pk_fp8_f32 v118, v113, v114
	s_and_b64 vcc, exec, vcc
	s_and_b32 s24, s58, 31
	ds_write_b16 v112, v115
	ds_write_b16 v112, v116 offset:68
	ds_write_b16 v112, v117 offset:136
	ds_write_b16 v112, v118 offset:204
	s_cbranch_vccnz .LBB4_809
	s_lshl_b32 s8, s24, 7
	s_lshl_b32 s9, s58, 6
	s_and_b32 s8, s8, 0xf00
	s_and_b32 s9, s9, 64
	s_or_b32 s20, s8, s9
	s_cbranch_execnz .LBB4_803

; #define AT_SBAR() __builtin_amdgcn_sched_barrier(0)
; #define AT_CV_READ() do { if (cv.pend) { const char* t_ = lds + cv_lr + ((cv.ci - 1) & 1) * CV_TILE; cvr0 = *(const unsigned*)t_; cvr1 = *(const unsigned*)(t_ + 4); } } while (0)
; #define AT_CV_STORE() do { if (cv.pend) { GAS unsigned char* gd_ = (GAS unsigned char*)cv.sdst; unsigned o_ = cv_sto; asm volatile("" : "+s"(gd_), "+v"(o_)); __builtin_nontemporal_store((u32x2){cvr0, cvr1}, (GAS u32x2*)(gd_ + (size_t)o_)); cv.pend = 0; } } while (0)
; DI void attn_pass(const Frame& F, CvRide& cv, const bf16_t* __restrict__ Qb, const bf16_t* __restrict__ Kh, const bf16_t* __restrict__ Vh, char* lds, f32x16 (&o)[4], float& l_out, const int wave_s) {
;     ...
;     for (int j = 1; j + 2 < NT; j += 2) {
;         AT_STEP(pB0, pB1, pA0, pA1, alB, alA, j, true);
;         AT_STEP(pA0, pA1, pB0, pB1, alA, alB, j + 1, true);
;     }
;     AT_STEP(pB0, pB1, pA0, pA1, alB, alA, NT - 1, false);
;     AT_CV_READ(); AT_CV_STORE();
;     finishSM(pB0, pB1, alB, l_reg, pa0, pa1, pa2, pa3); AT_SBAR();
;     pv_all(o, vb0 + s_prev * SHM_V, pa0, pa1, pa2, pa3);
.LBB4_812:
	v_mov_b64_e32 v[64:65], v[80:81]
	v_mov_b64_e32 v[66:67], v[82:83]
	v_mov_b64_e32 v[68:69], v[84:85]
	v_mov_b64_e32 v[70:71], v[86:87]
	v_mov_b64_e32 v[72:73], v[88:89]
	v_mov_b64_e32 v[74:75], v[90:91]
	v_mov_b64_e32 v[76:77], v[92:93]
	v_mov_b64_e32 v[78:79], v[94:95]
	s_and_b64 vcc, exec, s[22:23]
	s_cbranch_vccz .LBB4_814
	s_andn2_b32 s15, 1, s58
	s_mulk_i32 s15, 0x1100
	v_add_u32_e32 v80, s15, v194
	ds_read2_b32 v[184:185], v80 offset1:1

; #define AT_SBAR() __builtin_amdgcn_sched_barrier(0)
; template <int D0> DI void pv_one(f32x16& od, int vb, bf16x8 pa0, bf16x8 pa1, bf16x8 pa2, bf16x8 pa3) {
;     const s16x4 l0 = tr_read<v_rd_off(D0, 0, 0)>(vb), h0 = tr_read<v_rd_off(D0, 0, 1)>(vb), l1 = tr_read<v_rd_off(D0, 1, 0)>(vb), h1 = tr_read<v_rd_off(D0, 1, 1)>(vb);
;     const s16x4 l2 = tr_read<v_rd_off(D0, 2, 0)>(vb), h2 = tr_read<v_rd_off(D0, 2, 1)>(vb), l3 = tr_read<v_rd_off(D0, 3, 0)>(vb), h3 = tr_read<v_rd_off(D0, 3, 1)>(vb);
;     asm volatile("s_waitcnt lgkmcnt(0)" ::: "memory"); AT_SBAR();
;     ...
;     od = __builtin_amdgcn_mfma_f32_32x32x16_bf16(AT_PK(l0, h0), pa0, od, 0, 0, 0);
;     od = __builtin_amdgcn_mfma_f32_32x32x16_bf16(AT_PK(l1, h1), pa1, od, 0, 0, 0);
;     od = __builtin_amdgcn_mfma_f32_32x32x16_bf16(AT_PK(l2, h2), pa2, od, 0, 0, 0);
;     od = __builtin_amdgcn_mfma_f32_32x32x16_bf16(AT_PK(l3, h3), pa3, od, 0, 0, 0);
;     ...
; }
; DI void pv_all_sm(f32x16* o, int vb, bf16x8 pa0, bf16x8 pa1, bf16x8 pa2, bf16x8 pa3, f32x16& p0, f32x16& p1, float& m_ref, f32x16& negm, float& alpha) {
;     pv_one<0>(o[0], vb, pa0, pa1, pa2, pa3);
;     float pmax = p0[0];
; #pragma unroll
;     for (int r = 1; r < 16; ++r) pmax = fmaxf(pmax, p0[r]);
;     pv_one<1>(o[1], vb, pa0, pa1, pa2, pa3);
; #pragma unroll
;     for (int r = 0; r < 16; ++r) pmax = fmaxf(pmax, p1[r]);
;     { auto rr = __builtin_amdgcn_permlane32_swap(__float_as_uint(pmax), __float_as_uint(pmax), false, false); pmax = fmaxf(__uint_as_float(rr[0]), __uint_as_float(rr[1])); }
;     pv_one<2>(o[2], vb, pa0, pa1, pa2, pa3);
;     alpha = 1.f;
;     if (__builtin_expect(!__all(pmax <= THRL), 0)) {
;         const float dl = fmaxf(pmax, 0.f); m_ref += dl; alpha = __builtin_amdgcn_exp2f(-dl);
; #pragma unroll
;         for (int r = 0; r < 16; ++r) { p0[r] -= dl; p1[r] -= dl; }
; #pragma unroll
;         for (int r = 0; r < 16; ++r) negm[r] = -m_ref;
;     }
;     pv_one<3>(o[3], vb, pa0, pa1, pa2, pa3);
; #pragma unroll
;     for (int r = 0; r < 16; ++r) p0[r] = __builtin_amdgcn_exp2f(p0[r]);
; }
; DI void attn_pass(const Frame& F, CvRide& cv, const bf16_t* __restrict__ Qb, const bf16_t* __restrict__ Kh, const bf16_t* __restrict__ Vh, char* lds, f32x16 (&o)[4], float& l_out, const int wave_s) {
;     ...
;     const unsigned cv_ldo = (unsigned)(((tid >> 4) * 2 * 2048 + (tid & 15) * 4) * 4), cv_sto = (unsigned)((tid >> 3) * 2048 + 8 * (tid & 7));
.LBB4_851:
	s_lshl_b32 s65, s63, 14
	v_add_u32_e32 v182, s65, v191
	ds_read_b64_tr_b16 v[64:65], v182 offset:0
	ds_read_b64_tr_b16 v[66:67], v182 offset:0x800
	ds_read_b64_tr_b16 v[68:69], v182 offset:0x1000
	ds_read_b64_tr_b16 v[70:71], v182 offset:0x1800
	ds_read_b64_tr_b16 v[72:73], v182 offset:0x2000
	ds_read_b64_tr_b16 v[74:75], v182 offset:0x2800
	ds_read_b64_tr_b16 v[76:77], v182 offset:0x3000
	ds_read_b64_tr_b16 v[78:79], v182 offset:0x3800
	s_waitcnt lgkmcnt(0)
	s_nop 0
	v_mfma_f32_32x32x16_bf16 v[32:47], v[64:67], v[96:99], v[32:47]
	v_max_f32_e32 v64, v128, v129
	v_max3_f32 v64, v64, v130, v131
	v_max3_f32 v64, v64, v132, v133
	v_max3_f32 v64, v64, v134, v135
	v_max3_f32 v64, v64, v136, v137
	v_mfma_f32_32x32x16_bf16 v[32:47], v[68:71], v[108:111], v[32:47]
	v_max3_f32 v64, v64, v138, v139
	v_max3_f32 v66, v64, v140, v141
	ds_read_b64_tr_b16 v[64:65], v182 offset:0x200
	v_max3_f32 v180, v66, v142, v143
	ds_read_b64_tr_b16 v[66:67], v182 offset:0xa00
	ds_read_b64_tr_b16 v[68:69], v182 offset:0x1200
	ds_read_b64_tr_b16 v[70:71], v182 offset:0x1a00
	v_mfma_f32_32x32x16_bf16 v[32:47], v[72:75], v[100:103], v[32:47]
	ds_read_b64_tr_b16 v[72:73], v182 offset:0x2200
	ds_read_b64_tr_b16 v[74:75], v182 offset:0x2a00
	ds_read_b64_tr_b16 v[214:215], v182 offset:0x3200
	ds_read_b64_tr_b16 v[216:217], v182 offset:0x3a00
	s_waitcnt lgkmcnt(0)
	v_mfma_f32_32x32x16_bf16 v[32:47], v[76:79], v[104:107], v[32:47]
	v_mfma_f32_32x32x16_bf16 v[48:63], v[64:67], v[96:99], v[48:63]
	v_max3_f32 v76, v180, v112, v113
	v_max3_f32 v64, v76, v114, v115
	ds_read_b64_tr_b16 v[66:67], v182 offset:0x400
	v_max3_f32 v64, v64, v116, v117
	v_max3_f32 v64, v64, v118, v119
	v_max3_f32 v64, v64, v120, v121
	v_max3_f32 v64, v64, v122, v123
	v_mfma_f32_32x32x16_bf16 v[48:63], v[68:71], v[108:111], v[48:63]
	ds_read_b64_tr_b16 v[68:69], v182 offset:0xc00
	ds_read_b64_tr_b16 v[70:71], v182 offset:0x1400
	v_max3_f32 v64, v64, v124, v125
	v_max3_f32 v64, v64, v126, v127
	v_mov_b32_e32 v65, v64
	s_nop 1
	v_permlane32_swap_b32_e32 v64, v65
	v_mfma_f32_32x32x16_bf16 v[48:63], v[72:75], v[100:103], v[48:63]
	ds_read_b64_tr_b16 v[72:73], v182 offset:0x1c00
	ds_read_b64_tr_b16 v[74:75], v182 offset:0x2400
	ds_read_b64_tr_b16 v[76:77], v182 offset:0x2c00
	ds_read_b64_tr_b16 v[218:219], v182 offset:0x3400
	ds_read_b64_tr_b16 v[220:221], v182 offset:0x3c00
	s_waitcnt lgkmcnt(0)
	v_mfma_f32_32x32x16_bf16 v[48:63], v[214:217], v[104:107], v[48:63]
	v_max_f32_e32 v64, v64, v65
	v_mfma_f32_32x32x16_bf16 v[16:31], v[66:69], v[96:99], v[16:31]
	v_cmp_ge_f32_e32 vcc, s15, v64
	s_cmp_eq_u64 vcc, exec
	v_mfma_f32_32x32x16_bf16 v[16:31], v[70:73], v[108:111], v[16:31]
	v_mfma_f32_32x32x16_bf16 v[16:31], v[74:77], v[100:103], v[16:31]
	v_mfma_f32_32x32x16_bf16 v[16:31], v[218:221], v[104:107], v[16:31]
	s_cbranch_scc0 .LBB4_884
	v_mov_b32_e32 v180, 1.0
.LBB4_853:
	ds_read_b64_tr_b16 v[214:215], v182 offset:0x600
	ds_read_b64_tr_b16 v[216:217], v182 offset:0xe00
	ds_read_b64_tr_b16 v[218:219], v182 offset:0x1600
	ds_read_b64_tr_b16 v[220:221], v182 offset:0x1e00
	ds_read_b64_tr_b16 v[222:223], v182 offset:0x2600
	ds_read_b64_tr_b16 v[224:225], v182 offset:0x2e00
	ds_read_b64_tr_b16 v[226:227], v182 offset:0x3600
	ds_read_b64_tr_b16 v[228:229], v182 offset:0x3e00
	s_waitcnt lgkmcnt(0)
	s_nop 0
	v_mfma_f32_32x32x16_bf16 v[0:15], v[214:217], v[96:99], v[0:15]
	v_exp_f32_e32 v182, v128
	v_exp_f32_e32 v230, v129
	v_exp_f32_e32 v231, v130
	v_exp_f32_e32 v232, v131
	s_lshl_b32 s2, s57, 14
	s_add_i32 s2, s2, 0
	s_lshl_b32 s3, s57, 13
	v_add_u32_e32 v96, s2, v199
	s_sub_i32 s76, s2, s3
	s_waitcnt vmcnt(0)
	v_add_u32_e32 v97, s2, v200
	v_mfma_f32_32x32x16_bf16 v[0:15], v[218:221], v[108:111], v[0:15]
	v_exp_f32_e32 v233, v132
	v_exp_f32_e32 v234, v133
	v_exp_f32_e32 v235, v134
	v_exp_f32_e32 v236, v135
	ds_write_b128 v96, v[176:179]
	v_add_u32_e32 v96, s76, v201
	ds_write_b128 v97, v[172:175]
	ds_write_b128 v96, v[168:171] offset:49152
	s_andn2_b64 s[2:3], exec, s[30:31]
	s_andn2_b64 vcc, exec, s[30:31]
	v_mfma_f32_32x32x16_bf16 v[0:15], v[222:225], v[100:103], v[0:15]
	v_exp_f32_e32 v237, v136
	v_exp_f32_e32 v238, v137
	v_exp_f32_e32 v239, v138
	v_exp_f32_e32 v240, v139
	v_mfma_f32_32x32x16_bf16 v[0:15], v[226:229], v[104:107], v[0:15]
	v_exp_f32_e32 v241, v140
	v_exp_f32_e32 v242, v141
	v_exp_f32_e32 v243, v142
	v_exp_f32_e32 v244, v143
	s_cbranch_vccnz .LBB4_858
	v_mul_f32_e32 v97, 0x44000000, v160
	v_mul_f32_e32 v98, 0x44000000, v164
	v_med3_f32 v97, v97, s56, v210
	v_med3_f32 v98, v98, s56, v210
	v_cvt_pk_fp8_f32 v99, v97, v98
	v_mul_f32_e32 v97, 0x44000000, v161
	v_mul_f32_e32 v98, 0x44000000, v165
	v_med3_f32 v97, v97, s56, v210
	v_med3_f32 v98, v98, s56, v210
	v_cvt_pk_fp8_f32 v100, v97, v98
	v_mul_f32_e32 v97, 0x44000000, v162
	v_mul_f32_e32 v98, 0x44000000, v166
	v_med3_f32 v97, v97, s56, v210
	v_med3_f32 v98, v98, s56, v210
	s_bitcmp1_b32 s58, 0
	v_cvt_pk_fp8_f32 v101, v97, v98
	v_mul_f32_e32 v97, 0x44000000, v163
	v_mul_f32_e32 v98, 0x44000000, v167
	s_cselect_b32 s8, 0x1100, 0
	v_med3_f32 v97, v97, s56, v210
	v_med3_f32 v98, v98, s56, v210
	v_cmp_eq_u32_e32 vcc, 0, v181
	v_add_u32_e32 v96, s8, v190
	v_cvt_pk_fp8_f32 v102, v97, v98
	s_and_b64 vcc, exec, vcc
	s_and_b32 s30, s58, 31
	ds_write_b16 v96, v99
	ds_write_b16 v96, v100 offset:68
	ds_write_b16 v96, v101 offset:136
	ds_write_b16 v96, v102 offset:204
	s_cbranch_vccnz .LBB4_882
	s_lshl_b32 s8, s30, 7
	s_lshl_b32 s9, s58, 6
	s_and_b32 s8, s8, 0xf00
	s_and_b32 s9, s9, 64
	s_or_b32 s26, s8, s9
	s_cbranch_execnz .LBB4_857

; DI void finishSM(f32x16& p0, f32x16& p1, float alpha, float& l_reg, bf16x8& pa0, bf16x8& pa1, bf16x8& pa2, bf16x8& pa3) {
; #pragma unroll
;     for (int r = 0; r < 16; ++r) p1[r] = __builtin_amdgcn_exp2f(p1[r]);
;     float ps = 0;
; #pragma unroll
;     for (int r = 0; r < 16; ++r) ps += p0[r];
; #pragma unroll
;     for (int r = 0; r < 16; ++r) ps += p1[r];
;     { auto rr = __builtin_amdgcn_permlane32_swap(__float_as_uint(ps), __float_as_uint(ps), false, false); ps = __uint_as_float(rr[0]) + __uint_as_float(rr[1]); }
;     l_reg = l_reg * alpha + ps;
;     ...
;     AT_PK4(p0, 0, pa0); AT_PK4(p0, 8, pa1); AT_PK4(p1, 0, pa2); AT_PK4(p1, 8, pa3);
;     ...
; }
; DI void qkt(f32x16& p0, f32x16& p1, const char* Ks, const bf16x8* qr, const f32x16& negm, int r32, int hi) {
; #pragma unroll
;     for (int d0 = 0; d0 < 4; ++d0) { const int cb = (d0 * 16 + hi * 8) * 2;
;         const bf16x8 b0 = *reinterpret_cast<const bf16x8*>(Ks + AT_KSWZ(r32, cb));
;         const bf16x8 b1 = *reinterpret_cast<const bf16x8*>(Ks + AT_KSWZ(32 + r32, cb));
;         p0 = __builtin_amdgcn_mfma_f32_32x32x16_bf16(b0, qr[d0], d0 == 0 ? negm : p0, 0, 0, 0);
;         p1 = __builtin_amdgcn_mfma_f32_32x32x16_bf16(b1, qr[d0], d0 == 0 ? negm : p1, 0, 0, 0); }
; }
; DI void attn_pass(const Frame& F, CvRide& cv, const bf16_t* __restrict__ Qb, const bf16_t* __restrict__ Kh, const bf16_t* __restrict__ Vh, char* lds, f32x16 (&o)[4], float& l_out, const int wave_s) {
;     ...
;     const unsigned cv_ldo = (unsigned)(((tid >> 4) * 2 * 2048 + (tid & 15) * 4) * 4), cv_sto = (unsigned)((tid >> 3) * 2048 + 8 * (tid & 7));
;     const int cv_lw = OFF_CV + (4 * (tid & 15)) * 68 + 2 * (tid >> 4), cv_lr = OFF_CV + (tid >> 3) * 68 + 8 * (tid & 7);
;     f32x4 cvA = f32x4{}, cvB = f32x4{}; unsigned cvr0 = 0, cvr1 = 0;
.LBB4_870:
	v_add_u32_e32 v100, s76, v203
	ds_read_b128 v[96:99], v100 offset:49152
	ds_read_b128 v[168:171], v100 offset:53248
	v_add_u32_e32 v101, s76, v204
	v_add_u32_e32 v102, s76, v205
	v_add_u32_e32 v103, s76, v206
	ds_read_b128 v[172:175], v101 offset:49152
	ds_read_b128 v[176:179], v101 offset:53248
	ds_read_b128 v[214:217], v102 offset:49152
	ds_read_b128 v[218:221], v102 offset:53248
	ds_read_b128 v[222:225], v103 offset:49152
	ds_read_b128 v[226:229], v103 offset:53248
	v_exp_f32_e32 v112, v112
	v_exp_f32_e32 v113, v113
	v_exp_f32_e32 v114, v114
	s_waitcnt lgkmcnt(7)
	v_mfma_f32_32x32x16_bf16 v[128:143], v[96:99], v[156:159], v[80:95]
	v_exp_f32_e32 v115, v115
	v_exp_f32_e32 v116, v116
	v_exp_f32_e32 v117, v117
	v_exp_f32_e32 v118, v118
	v_exp_f32_e32 v119, v119
	s_waitcnt lgkmcnt(6)
	v_mfma_f32_32x32x16_bf16 v[96:111], v[168:171], v[156:159], v[80:95]
	v_exp_f32_e32 v168, v120
	v_add_f32_e32 v120, 0, v182
	v_add_f32_e32 v120, v230, v120
	v_add_f32_e32 v120, v231, v120
	v_add_f32_e32 v120, v232, v120
	v_add_f32_e32 v120, v233, v120
	v_add_f32_e32 v120, v234, v120
	v_add_f32_e32 v120, v235, v120
	v_add_f32_e32 v120, v236, v120
	v_add_f32_e32 v120, v237, v120
	v_add_f32_e32 v120, v238, v120
	s_waitcnt lgkmcnt(5)
	v_mfma_f32_32x32x16_bf16 v[128:143], v[172:175], v[152:155], v[128:143]
	v_add_f32_e32 v120, v239, v120
	v_add_f32_e32 v120, v240, v120
	v_add_f32_e32 v120, v241, v120
	v_add_f32_e32 v120, v242, v120
	v_add_f32_e32 v120, v243, v120
	v_add_f32_e32 v120, v244, v120
	v_add_f32_e32 v120, v112, v120
	s_waitcnt lgkmcnt(4)
	v_mfma_f32_32x32x16_bf16 v[96:111], v[176:179], v[152:155], v[96:111]
	v_add_f32_e32 v120, v113, v120
	v_add_f32_e32 v120, v114, v120
	v_add_f32_e32 v120, v115, v120
	v_add_f32_e32 v120, v116, v120
	v_exp_f32_e32 v169, v121
	v_add_f32_e32 v120, v117, v120
	v_exp_f32_e32 v170, v122
	s_waitcnt lgkmcnt(3)
	v_mfma_f32_32x32x16_bf16 v[128:143], v[214:217], v[148:151], v[128:143]
	v_add_f32_e32 v120, v118, v120
	v_exp_f32_e32 v171, v123
	v_add_f32_e32 v120, v119, v120
	v_exp_f32_e32 v172, v124
	v_add_f32_e32 v120, v168, v120
	v_exp_f32_e32 v173, v125
	v_add_f32_e32 v120, v169, v120
	s_waitcnt lgkmcnt(2)
	v_mfma_f32_32x32x16_bf16 v[96:111], v[218:221], v[148:151], v[96:111]
	v_exp_f32_e32 v174, v126
	v_add_f32_e32 v120, v170, v120
	v_exp_f32_e32 v175, v127
	v_add_f32_e32 v120, v171, v120
	v_add_f32_e32 v120, v172, v120
	v_add_f32_e32 v120, v173, v120
	v_add_f32_e32 v120, v174, v120
	s_waitcnt lgkmcnt(1)
	v_mfma_f32_32x32x16_bf16 v[128:143], v[222:225], v[144:147], v[128:143]
	v_add_f32_e32 v213, v175, v120
	v_mov_b32_e32 v214, v213
	v_cvt_pk_bf16_f32 v120, v182, v230
	v_cvt_pk_bf16_f32 v121, v231, v232
	v_cvt_pk_bf16_f32 v122, v233, v234
	v_cvt_pk_bf16_f32 v123, v235, v236
	v_cvt_pk_bf16_f32 v124, v237, v238
	s_waitcnt lgkmcnt(0)
	v_mfma_f32_32x32x16_bf16 v[96:111], v[226:229], v[144:147], v[96:111]
	v_cvt_pk_bf16_f32 v125, v239, v240
	v_cvt_pk_bf16_f32 v126, v241, v242
	v_cvt_pk_bf16_f32 v127, v243, v244
	v_cvt_pk_bf16_f32 v112, v112, v113
	v_cvt_pk_bf16_f32 v113, v114, v115
	v_cvt_pk_bf16_f32 v114, v116, v117
	v_cvt_pk_bf16_f32 v115, v118, v119
	v_cvt_pk_bf16_f32 v116, v168, v169
	v_cvt_pk_bf16_f32 v117, v170, v171
	v_cvt_pk_bf16_f32 v118, v172, v173
	v_cvt_pk_bf16_f32 v119, v174, v175
	v_permlane32_swap_b32_e32 v213, v214
	v_permlane32_swap_b32_e32 v120, v122
	v_permlane32_swap_b32_e32 v121, v123
	v_permlane32_swap_b32_e32 v124, v126
	v_permlane32_swap_b32_e32 v125, v127
	v_permlane32_swap_b32_e32 v112, v114
	v_permlane32_swap_b32_e32 v113, v115
	v_permlane32_swap_b32_e32 v116, v118
	v_permlane32_swap_b32_e32 v117, v119
	s_add_u32 s34, s66, 0x2380c000
	s_addc_u32 s35, s67, 0
	s_add_u32 s66, s66, 0x2380e000
	s_addc_u32 s67, s67, 0
	s_add_u32 s74, s74, 0x21806000
	s_addc_u32 s75, s75, 0
	v_mov_b32_e32 v168, v197
	v_mov_b32_e32 v169, v196
	global_load_dwordx4 v[176:179], v169, s[34:35]
	global_load_dwordx4 v[172:175], v169, s[66:67]
	s_nop 0
	global_load_dwordx4 v[168:171], v168, s[74:75]
	s_and_b64 vcc, exec, s[2:3]
	s_cbranch_vccnz .LBB4_872
	v_mov_b32_e32 v182, v188
	s_mov_b64 s[2:3], s[8:9]
	global_store_dwordx2 v182, v[184:185], s[2:3] nt
; #define AT_SBAR() __builtin_amdgcn_sched_barrier(0)
; template <int D0> DI void pv_one(f32x16& od, int vb, bf16x8 pa0, bf16x8 pa1, bf16x8 pa2, bf16x8 pa3) {
;     const s16x4 l0 = tr_read<v_rd_off(D0, 0, 0)>(vb), h0 = tr_read<v_rd_off(D0, 0, 1)>(vb), l1 = tr_read<v_rd_off(D0, 1, 0)>(vb), h1 = tr_read<v_rd_off(D0, 1, 1)>(vb);
;     const s16x4 l2 = tr_read<v_rd_off(D0, 2, 0)>(vb), h2 = tr_read<v_rd_off(D0, 2, 1)>(vb), l3 = tr_read<v_rd_off(D0, 3, 0)>(vb), h3 = tr_read<v_rd_off(D0, 3, 1)>(vb);
;     asm volatile("s_waitcnt lgkmcnt(0)" ::: "memory"); AT_SBAR();
;     ...
;     od = __builtin_amdgcn_mfma_f32_32x32x16_bf16(AT_PK(l0, h0), pa0, od, 0, 0, 0);
;     od = __builtin_amdgcn_mfma_f32_32x32x16_bf16(AT_PK(l1, h1), pa1, od, 0, 0, 0);
;     od = __builtin_amdgcn_mfma_f32_32x32x16_bf16(AT_PK(l2, h2), pa2, od, 0, 0, 0);
;     od = __builtin_amdgcn_mfma_f32_32x32x16_bf16(AT_PK(l3, h3), pa3, od, 0, 0, 0);
;     ...
; }
; DI void pv_all_sm(f32x16* o, int vb, bf16x8 pa0, bf16x8 pa1, bf16x8 pa2, bf16x8 pa3, f32x16& p0, f32x16& p1, float& m_ref, f32x16& negm, float& alpha) {
;     pv_one<0>(o[0], vb, pa0, pa1, pa2, pa3);
;     float pmax = p0[0];
; #pragma unroll
;     for (int r = 1; r < 16; ++r) pmax = fmaxf(pmax, p0[r]);
;     pv_one<1>(o[1], vb, pa0, pa1, pa2, pa3);
; #pragma unroll
;     for (int r = 0; r < 16; ++r) pmax = fmaxf(pmax, p1[r]);
;     { auto rr = __builtin_amdgcn_permlane32_swap(__float_as_uint(pmax), __float_as_uint(pmax), false, false); pmax = fmaxf(__uint_as_float(rr[0]), __uint_as_float(rr[1])); }
;     pv_one<2>(o[2], vb, pa0, pa1, pa2, pa3);
;     alpha = 1.f;
;     if (__builtin_expect(!__all(pmax <= THRL), 0)) {
;         const float dl = fmaxf(pmax, 0.f); m_ref += dl; alpha = __builtin_amdgcn_exp2f(-dl);
; #pragma unroll
;         for (int r = 0; r < 16; ++r) { p0[r] -= dl; p1[r] -= dl; }
; #pragma unroll
;         for (int r = 0; r < 16; ++r) negm[r] = -m_ref;
;     }
;     pv_one<3>(o[3], vb, pa0, pa1, pa2, pa3);
; #pragma unroll
;     for (int r = 0; r < 16; ++r) p0[r] = __builtin_amdgcn_exp2f(p0[r]);
; }
; DI void attn_pass(const Frame& F, CvRide& cv, const bf16_t* __restrict__ Qb, const bf16_t* __restrict__ Kh, const bf16_t* __restrict__ Vh, char* lds, f32x16 (&o)[4], float& l_out, const int wave_s) {
;     ...
;     const unsigned cv_ldo = (unsigned)(((tid >> 4) * 2 * 2048 + (tid & 15) * 4) * 4), cv_sto = (unsigned)((tid >> 3) * 2048 + 8 * (tid & 7));
.LBB4_872:
	v_lshl_add_u32 v215, s64, 14, v191
	ds_read_b64_tr_b16 v[216:217], v215 offset:0
	ds_read_b64_tr_b16 v[218:219], v215 offset:0x800
	ds_read_b64_tr_b16 v[220:221], v215 offset:0x1000
	ds_read_b64_tr_b16 v[222:223], v215 offset:0x1800
	ds_read_b64_tr_b16 v[224:225], v215 offset:0x2000
	ds_read_b64_tr_b16 v[226:227], v215 offset:0x2800
	ds_read_b64_tr_b16 v[228:229], v215 offset:0x3000
	ds_read_b64_tr_b16 v[230:231], v215 offset:0x3800
	s_waitcnt lgkmcnt(0)
	s_nop 0
	v_mfma_f32_32x32x16_bf16 v[32:47], v[216:219], v[120:123], v[32:47]
	v_max_f32_e32 v182, v128, v129
	ds_read_b64_tr_b16 v[216:217], v215 offset:0x200
	ds_read_b64_tr_b16 v[218:219], v215 offset:0xa00
	v_max3_f32 v182, v182, v130, v131
	v_max3_f32 v182, v182, v132, v133
	v_mfma_f32_32x32x16_bf16 v[32:47], v[220:223], v[124:127], v[32:47]
	ds_read_b64_tr_b16 v[220:221], v215 offset:0x1200
	ds_read_b64_tr_b16 v[222:223], v215 offset:0x1a00
	v_max3_f32 v182, v182, v134, v135
	v_max3_f32 v182, v182, v136, v137
	v_max3_f32 v182, v182, v138, v139
	v_max3_f32 v182, v182, v140, v141
	v_max3_f32 v182, v182, v142, v143
	v_mfma_f32_32x32x16_bf16 v[32:47], v[224:227], v[112:115], v[32:47]
	ds_read_b64_tr_b16 v[224:225], v215 offset:0x2200
	ds_read_b64_tr_b16 v[226:227], v215 offset:0x2a00
	ds_read_b64_tr_b16 v[232:233], v215 offset:0x3200
	ds_read_b64_tr_b16 v[234:235], v215 offset:0x3a00
	s_waitcnt lgkmcnt(0)
	v_mfma_f32_32x32x16_bf16 v[32:47], v[228:231], v[116:119], v[32:47]
	v_mfma_f32_32x32x16_bf16 v[48:63], v[216:219], v[120:123], v[48:63]
	v_max3_f32 v182, v182, v96, v97
	v_max3_f32 v182, v182, v98, v99
	ds_read_b64_tr_b16 v[218:219], v215 offset:0x400
	v_max3_f32 v182, v182, v100, v101
	v_max3_f32 v182, v182, v102, v103
	v_max3_f32 v182, v182, v104, v105
	v_max3_f32 v182, v182, v106, v107
	v_mfma_f32_32x32x16_bf16 v[48:63], v[220:223], v[124:127], v[48:63]
	ds_read_b64_tr_b16 v[220:221], v215 offset:0xc00
	ds_read_b64_tr_b16 v[222:223], v215 offset:0x1400
	v_max3_f32 v182, v182, v108, v109
	v_max3_f32 v182, v182, v110, v111
	v_mov_b32_e32 v216, v182
	s_nop 1
	v_permlane32_swap_b32_e32 v182, v216
	v_mfma_f32_32x32x16_bf16 v[48:63], v[224:227], v[112:115], v[48:63]
	ds_read_b64_tr_b16 v[224:225], v215 offset:0x1c00
	ds_read_b64_tr_b16 v[226:227], v215 offset:0x2400
	ds_read_b64_tr_b16 v[228:229], v215 offset:0x2c00
	ds_read_b64_tr_b16 v[236:237], v215 offset:0x3400
	ds_read_b64_tr_b16 v[238:239], v215 offset:0x3c00
	s_waitcnt lgkmcnt(0)
	v_mfma_f32_32x32x16_bf16 v[48:63], v[232:235], v[116:119], v[48:63]
	v_max_f32_e32 v216, v182, v216
	v_mfma_f32_32x32x16_bf16 v[16:31], v[218:221], v[120:123], v[16:31]
	v_cmp_ge_f32_e32 vcc, s15, v216
	s_cmp_eq_u64 vcc, exec
	v_mov_b32_e32 v182, 1.0
	v_mfma_f32_32x32x16_bf16 v[16:31], v[222:225], v[124:127], v[16:31]
	v_mfma_f32_32x32x16_bf16 v[16:31], v[226:229], v[112:115], v[16:31]
	v_mfma_f32_32x32x16_bf16 v[16:31], v[236:239], v[116:119], v[16:31]
	s_cbranch_scc0 .LBB4_885
.LBB4_873:
	ds_read_b64_tr_b16 v[216:217], v215 offset:0x600
	ds_read_b64_tr_b16 v[218:219], v215 offset:0xe00
	ds_read_b64_tr_b16 v[220:221], v215 offset:0x1600
	ds_read_b64_tr_b16 v[222:223], v215 offset:0x1e00
	ds_read_b64_tr_b16 v[224:225], v215 offset:0x2600
	ds_read_b64_tr_b16 v[226:227], v215 offset:0x2e00
	ds_read_b64_tr_b16 v[228:229], v215 offset:0x3600
	ds_read_b64_tr_b16 v[230:231], v215 offset:0x3e00
	s_waitcnt lgkmcnt(0)
	s_nop 0
	v_mfma_f32_32x32x16_bf16 v[0:15], v[216:219], v[120:123], v[0:15]
	s_add_i32 s2, s65, 0
	v_add_u32_e32 v120, s2, v199
	s_waitcnt vmcnt(0)
	ds_write_b128 v120, v[176:179]
	s_mov_b32 s26, 0
	s_andn2_b64 vcc, exec, s[30:31]
	v_mfma_f32_32x32x16_bf16 v[0:15], v[220:223], v[124:127], v[0:15]
	v_mfma_f32_32x32x16_bf16 v[0:15], v[224:227], v[112:115], v[0:15]
	v_add_u32_e32 v112, s2, v200
	ds_write_b128 v112, v[172:175]
	v_lshl_add_u32 v112, s63, 13, v202
	ds_write_b128 v112, v[168:171] offset:49152
	s_andn2_b64 s[2:3], exec, s[30:31]
	v_mfma_f32_32x32x16_bf16 v[0:15], v[228:231], v[116:119], v[0:15]
	s_cbranch_vccnz .LBB4_878
	v_mul_f32_e32 v113, 0x44000000, v160
	v_mul_f32_e32 v114, 0x44000000, v164
	v_med3_f32 v113, v113, s56, v210
	v_med3_f32 v114, v114, s56, v210
	v_cvt_pk_fp8_f32 v115, v113, v114
	v_mul_f32_e32 v113, 0x44000000, v161
	v_mul_f32_e32 v114, 0x44000000, v165
	v_med3_f32 v113, v113, s56, v210
	v_med3_f32 v114, v114, s56, v210
	v_cvt_pk_fp8_f32 v116, v113, v114
	v_mul_f32_e32 v113, 0x44000000, v162
	v_mul_f32_e32 v114, 0x44000000, v166
	v_med3_f32 v113, v113, s56, v210
	v_med3_f32 v114, v114, s56, v210
	s_bitcmp1_b32 s58, 0
	v_cvt_pk_fp8_f32 v117, v113, v114
	v_mul_f32_e32 v113, 0x44000000, v163
	v_mul_f32_e32 v114, 0x44000000, v167
	s_cselect_b32 s8, 0x1100, 0
	v_med3_f32 v113, v113, s56, v210
	v_med3_f32 v114, v114, s56, v210
	v_cmp_eq_u32_e32 vcc, 0, v181
	v_add_u32_e32 v112, s8, v190
	v_cvt_pk_fp8_f32 v118, v113, v114
	s_and_b64 vcc, exec, vcc
	s_and_b32 s34, s58, 31
	ds_write_b16 v112, v115
	ds_write_b16 v112, v116 offset:68
	ds_write_b16 v112, v117 offset:136
	ds_write_b16 v112, v118 offset:204
	s_cbranch_vccnz .LBB4_883
	s_lshl_b32 s8, s34, 7
	s_lshl_b32 s9, s58, 6
	s_and_b32 s8, s8, 0xf00
	s_and_b32 s9, s9, 64
	s_or_b32 s26, s8, s9
	s_cbranch_execnz .LBB4_877

; #define AT_SBAR() __builtin_amdgcn_sched_barrier(0)
; #define AT_CV_READ() do { if (cv.pend) { const char* t_ = lds + cv_lr + ((cv.ci - 1) & 1) * CV_TILE; cvr0 = *(const unsigned*)t_; cvr1 = *(const unsigned*)(t_ + 4); } } while (0)
; #define AT_CV_STORE() do { if (cv.pend) { GAS unsigned char* gd_ = (GAS unsigned char*)cv.sdst; unsigned o_ = cv_sto; asm volatile("" : "+s"(gd_), "+v"(o_)); __builtin_nontemporal_store((u32x2){cvr0, cvr1}, (GAS u32x2*)(gd_ + (size_t)o_)); cv.pend = 0; } } while (0)
; DI void attn_pass(const Frame& F, CvRide& cv, const bf16_t* __restrict__ Qb, const bf16_t* __restrict__ Kh, const bf16_t* __restrict__ Vh, char* lds, f32x16 (&o)[4], float& l_out, const int wave_s) {
;     ...
;     AT_STEP(pB0, pB1, pA0, pA1, alB, alA, NT - 1, false);
;     AT_CV_READ(); AT_CV_STORE();
;     finishSM(pB0, pB1, alB, l_reg, pa0, pa1, pa2, pa3); AT_SBAR();
.LBB4_886:
	v_mov_b64_e32 v[64:65], v[80:81]
	v_mov_b64_e32 v[66:67], v[82:83]
	v_mov_b64_e32 v[68:69], v[84:85]
	v_mov_b64_e32 v[70:71], v[86:87]
	v_mov_b64_e32 v[72:73], v[88:89]
	v_mov_b64_e32 v[74:75], v[90:91]
	v_mov_b64_e32 v[76:77], v[92:93]
	v_mov_b64_e32 v[78:79], v[94:95]
	s_and_b64 vcc, exec, s[30:31]
	s_cbranch_vccz .LBB4_888
	s_andn2_b32 s15, 1, s58
	s_mulk_i32 s15, 0x1100
	v_add_u32_e32 v80, s15, v189
	ds_read2_b32 v[184:185], v80 offset1:1

; #define AT_SBAR() __builtin_amdgcn_sched_barrier(0)
; template <int OFF> DI s16x4 tr_read(int vb) { s16x4 r; asm volatile("ds_read_b64_tr_b16 %0, %1 offset:%2" : "=&v"(r) : "v"(vb), "i"(OFF) : "memory"); return r; }
; template <int D0> DI void pv_one(f32x16& od, int vb, bf16x8 pa0, bf16x8 pa1, bf16x8 pa2, bf16x8 pa3) {
;     const s16x4 l0 = tr_read<v_rd_off(D0, 0, 0)>(vb), h0 = tr_read<v_rd_off(D0, 0, 1)>(vb), l1 = tr_read<v_rd_off(D0, 1, 0)>(vb), h1 = tr_read<v_rd_off(D0, 1, 1)>(vb);
;     const s16x4 l2 = tr_read<v_rd_off(D0, 2, 0)>(vb), h2 = tr_read<v_rd_off(D0, 2, 1)>(vb), l3 = tr_read<v_rd_off(D0, 3, 0)>(vb), h3 = tr_read<v_rd_off(D0, 3, 1)>(vb);
;     asm volatile("s_waitcnt lgkmcnt(0)" ::: "memory"); AT_SBAR();
;     ...
;     od = __builtin_amdgcn_mfma_f32_32x32x16_bf16(AT_PK(l0, h0), pa0, od, 0, 0, 0);
;     od = __builtin_amdgcn_mfma_f32_32x32x16_bf16(AT_PK(l1, h1), pa1, od, 0, 0, 0);
;     od = __builtin_amdgcn_mfma_f32_32x32x16_bf16(AT_PK(l2, h2), pa2, od, 0, 0, 0);
;     od = __builtin_amdgcn_mfma_f32_32x32x16_bf16(AT_PK(l3, h3), pa3, od, 0, 0, 0);
;     ...
; }
; DI void attn_pass(const Frame& F, CvRide& cv, const bf16_t* __restrict__ Qb, const bf16_t* __restrict__ Kh, const bf16_t* __restrict__ Vh, char* lds, f32x16 (&o)[4], float& l_out, const int wave_s) {
;     ...
;     const unsigned cv_ldo = (unsigned)(((tid >> 4) * 2 * 2048 + (tid & 15) * 4) * 4), cv_sto = (unsigned)((tid >> 3) * 2048 + 8 * (tid & 7));
;     const int cv_lw = OFF_CV + (4 * (tid & 15)) * 68 + 2 * (tid >> 4), cv_lr = OFF_CV + (tid >> 3) * 68 + 8 * (tid & 7);
;     f32x4 cvA = f32x4{}, cvB = f32x4{}; unsigned cvr0 = 0, cvr1 = 0;
.LBB4_927:
	ds_read_b64_tr_b16 v[218:219], v182 offset:0x600
	ds_read_b64_tr_b16 v[220:221], v182 offset:0xe00
	ds_read_b64_tr_b16 v[222:223], v182 offset:0x1600
	ds_read_b64_tr_b16 v[224:225], v182 offset:0x1e00
	ds_read_b64_tr_b16 v[226:227], v182 offset:0x2600
	ds_read_b64_tr_b16 v[228:229], v182 offset:0x2e00
	ds_read_b64_tr_b16 v[230:231], v182 offset:0x3600
	ds_read_b64_tr_b16 v[232:233], v182 offset:0x3e00
	s_waitcnt lgkmcnt(0)
	s_nop 0
	v_mfma_f32_32x32x16_bf16 v[0:15], v[218:221], v[96:99], v[0:15]
	v_exp_f32_e32 v182, v128
	v_exp_f32_e32 v234, v129
	v_exp_f32_e32 v235, v130
	v_exp_f32_e32 v236, v131
	s_lshl_b32 s2, s15, 14
	s_add_i32 s2, s2, 0
	s_lshl_b32 s3, s15, 13
	v_add_u32_e32 v96, s2, v203
	s_sub_i32 s54, s2, s3
	s_waitcnt vmcnt(0)
	v_add_u32_e32 v97, s2, v204
	v_mfma_f32_32x32x16_bf16 v[0:15], v[222:225], v[108:111], v[0:15]
	v_exp_f32_e32 v237, v132
	v_exp_f32_e32 v238, v133
	v_exp_f32_e32 v239, v134
	v_exp_f32_e32 v240, v135
	ds_write_b128 v96, v[176:179]
	v_add_u32_e32 v96, s54, v205
	ds_write_b128 v97, v[172:175]
	ds_write_b128 v96, v[168:171] offset:49152
	s_andn2_b64 s[2:3], exec, s[22:23]
	s_andn2_b64 vcc, exec, s[22:23]
	v_mfma_f32_32x32x16_bf16 v[0:15], v[226:229], v[100:103], v[0:15]
	v_exp_f32_e32 v241, v136
	v_exp_f32_e32 v242, v137
	v_exp_f32_e32 v243, v138
	v_exp_f32_e32 v244, v139
	v_mfma_f32_32x32x16_bf16 v[0:15], v[230:233], v[104:107], v[0:15]
	v_exp_f32_e32 v245, v140
	v_exp_f32_e32 v246, v141
	v_exp_f32_e32 v247, v142
	v_exp_f32_e32 v248, v143
	s_cbranch_vccnz .LBB4_932
	v_mul_f32_e32 v97, 0x44000000, v160
	v_mul_f32_e32 v98, 0x44000000, v164
	v_med3_f32 v97, v97, s28, v214
	v_med3_f32 v98, v98, s28, v214
	v_cvt_pk_fp8_f32 v99, v97, v98
	v_mul_f32_e32 v97, 0x44000000, v161
	v_mul_f32_e32 v98, 0x44000000, v165
	v_med3_f32 v97, v97, s28, v214
	v_med3_f32 v98, v98, s28, v214
	v_cvt_pk_fp8_f32 v100, v97, v98
	v_mul_f32_e32 v97, 0x44000000, v162
	v_mul_f32_e32 v98, 0x44000000, v166
	v_med3_f32 v97, v97, s28, v214
	v_med3_f32 v98, v98, s28, v214
	s_bitcmp1_b32 s58, 0
	v_cvt_pk_fp8_f32 v101, v97, v98
	v_mul_f32_e32 v97, 0x44000000, v163
	v_mul_f32_e32 v98, 0x44000000, v167
	s_cselect_b32 s8, 0x1100, 0
	v_med3_f32 v97, v97, s28, v214
	v_med3_f32 v98, v98, s28, v214
	v_cmp_eq_u32_e32 vcc, 0, v181
	v_add_u32_e32 v96, s8, v195
	v_cvt_pk_fp8_f32 v102, v97, v98
	s_and_b64 vcc, exec, vcc
	s_and_b32 s22, s58, 31
	ds_write_b16 v96, v99
	ds_write_b16 v96, v100 offset:68
	ds_write_b16 v96, v101 offset:136
	ds_write_b16 v96, v102 offset:204
	s_cbranch_vccnz .LBB4_956
	s_lshl_b32 s8, s22, 7
	s_lshl_b32 s9, s58, 6
	s_and_b32 s8, s8, 0xf00
	s_and_b32 s9, s9, 64
	s_or_b32 s18, s8, s9
	s_cbranch_execnz .LBB4_931

; DI void finishSM(f32x16& p0, f32x16& p1, float alpha, float& l_reg, bf16x8& pa0, bf16x8& pa1, bf16x8& pa2, bf16x8& pa3) {
; #pragma unroll
;     for (int r = 0; r < 16; ++r) p1[r] = __builtin_amdgcn_exp2f(p1[r]);
;     float ps = 0;
; #pragma unroll
;     for (int r = 0; r < 16; ++r) ps += p0[r];
; #pragma unroll
;     for (int r = 0; r < 16; ++r) ps += p1[r];
;     { auto rr = __builtin_amdgcn_permlane32_swap(__float_as_uint(ps), __float_as_uint(ps), false, false); ps = __uint_as_float(rr[0]) + __uint_as_float(rr[1]); }
;     l_reg = l_reg * alpha + ps;
;     ...
;     AT_PK4(p0, 0, pa0); AT_PK4(p0, 8, pa1); AT_PK4(p1, 0, pa2); AT_PK4(p1, 8, pa3);
;     ...
; }
; DI void qkt(f32x16& p0, f32x16& p1, const char* Ks, const bf16x8* qr, const f32x16& negm, int r32, int hi) {
; #pragma unroll
;     for (int d0 = 0; d0 < 4; ++d0) { const int cb = (d0 * 16 + hi * 8) * 2;
;         const bf16x8 b0 = *reinterpret_cast<const bf16x8*>(Ks + AT_KSWZ(r32, cb));
;         const bf16x8 b1 = *reinterpret_cast<const bf16x8*>(Ks + AT_KSWZ(32 + r32, cb));
;         p0 = __builtin_amdgcn_mfma_f32_32x32x16_bf16(b0, qr[d0], d0 == 0 ? negm : p0, 0, 0, 0);
;         p1 = __builtin_amdgcn_mfma_f32_32x32x16_bf16(b1, qr[d0], d0 == 0 ? negm : p1, 0, 0, 0); }
; }
; DI void attn_pass(const Frame& F, CvRide& cv, const bf16_t* __restrict__ Qb, const bf16_t* __restrict__ Kh, const bf16_t* __restrict__ Vh, char* lds, f32x16 (&o)[4], float& l_out, const int wave_s) {
;     ...
;     const unsigned cv_ldo = (unsigned)(((tid >> 4) * 2 * 2048 + (tid & 15) * 4) * 4), cv_sto = (unsigned)((tid >> 3) * 2048 + 8 * (tid & 7));
;     const int cv_lw = OFF_CV + (4 * (tid & 15)) * 68 + 2 * (tid >> 4), cv_lr = OFF_CV + (tid >> 3) * 68 + 8 * (tid & 7);
;     f32x4 cvA = f32x4{}, cvB = f32x4{}; unsigned cvr0 = 0, cvr1 = 0;
.LBB4_944:
	v_add_u32_e32 v100, s54, v207
	ds_read_b128 v[96:99], v100 offset:49152
	ds_read_b128 v[168:171], v100 offset:53248
	v_add_u32_e32 v101, s54, v208
	v_add_u32_e32 v102, s54, v209
	v_add_u32_e32 v103, s54, v210
	ds_read_b128 v[172:175], v101 offset:49152
	ds_read_b128 v[176:179], v101 offset:53248
	ds_read_b128 v[218:221], v102 offset:49152
	ds_read_b128 v[222:225], v102 offset:53248
	ds_read_b128 v[226:229], v103 offset:49152
	ds_read_b128 v[230:233], v103 offset:53248
	v_exp_f32_e32 v112, v112
	v_exp_f32_e32 v113, v113
	v_exp_f32_e32 v114, v114
	s_waitcnt lgkmcnt(7)
	v_mfma_f32_32x32x16_bf16 v[128:143], v[96:99], v[156:159], v[80:95]
	v_exp_f32_e32 v115, v115
	v_exp_f32_e32 v116, v116
	v_exp_f32_e32 v117, v117
	v_exp_f32_e32 v118, v118
	v_exp_f32_e32 v119, v119
	s_waitcnt lgkmcnt(6)
	v_mfma_f32_32x32x16_bf16 v[96:111], v[168:171], v[156:159], v[80:95]
	v_exp_f32_e32 v168, v120
	v_add_f32_e32 v120, 0, v182
	v_add_f32_e32 v120, v234, v120
	v_add_f32_e32 v120, v235, v120
	v_add_f32_e32 v120, v236, v120
	v_add_f32_e32 v120, v237, v120
	v_add_f32_e32 v120, v238, v120
	v_add_f32_e32 v120, v239, v120
	v_add_f32_e32 v120, v240, v120
	v_add_f32_e32 v120, v241, v120
	v_add_f32_e32 v120, v242, v120
	s_waitcnt lgkmcnt(5)
	v_mfma_f32_32x32x16_bf16 v[128:143], v[172:175], v[152:155], v[128:143]
	v_add_f32_e32 v120, v243, v120
	v_add_f32_e32 v120, v244, v120
	v_add_f32_e32 v120, v245, v120
	v_add_f32_e32 v120, v246, v120
	v_add_f32_e32 v120, v247, v120
	v_add_f32_e32 v120, v248, v120
	v_add_f32_e32 v120, v112, v120
	s_waitcnt lgkmcnt(4)
	v_mfma_f32_32x32x16_bf16 v[96:111], v[176:179], v[152:155], v[96:111]
	v_add_f32_e32 v120, v113, v120
	v_add_f32_e32 v120, v114, v120
	v_add_f32_e32 v120, v115, v120
	v_add_f32_e32 v120, v116, v120
	v_exp_f32_e32 v169, v121
	v_add_f32_e32 v120, v117, v120
	v_exp_f32_e32 v170, v122
	s_waitcnt lgkmcnt(3)
	v_mfma_f32_32x32x16_bf16 v[128:143], v[218:221], v[148:151], v[128:143]
	v_add_f32_e32 v120, v118, v120
	v_exp_f32_e32 v171, v123
	v_add_f32_e32 v120, v119, v120
	v_exp_f32_e32 v172, v124
	v_add_f32_e32 v120, v168, v120
	v_exp_f32_e32 v173, v125
	v_add_f32_e32 v120, v169, v120
	s_waitcnt lgkmcnt(2)
	v_mfma_f32_32x32x16_bf16 v[96:111], v[222:225], v[148:151], v[96:111]
	v_exp_f32_e32 v174, v126
	v_add_f32_e32 v120, v170, v120
	v_exp_f32_e32 v175, v127
	v_add_f32_e32 v120, v171, v120
	v_add_f32_e32 v120, v172, v120
	v_add_f32_e32 v120, v173, v120
	v_add_f32_e32 v120, v174, v120
	s_waitcnt lgkmcnt(1)
	v_mfma_f32_32x32x16_bf16 v[128:143], v[226:229], v[144:147], v[128:143]
	v_add_f32_e32 v217, v175, v120
	v_mov_b32_e32 v218, v217
	v_cvt_pk_bf16_f32 v120, v182, v234
	v_cvt_pk_bf16_f32 v121, v235, v236
	v_cvt_pk_bf16_f32 v122, v237, v238
	v_cvt_pk_bf16_f32 v123, v239, v240
	v_cvt_pk_bf16_f32 v124, v241, v242
	s_waitcnt lgkmcnt(0)
	v_mfma_f32_32x32x16_bf16 v[96:111], v[230:233], v[144:147], v[96:111]
	v_cvt_pk_bf16_f32 v125, v243, v244
	v_cvt_pk_bf16_f32 v126, v245, v246
	v_cvt_pk_bf16_f32 v127, v247, v248
	v_cvt_pk_bf16_f32 v112, v112, v113
	v_cvt_pk_bf16_f32 v113, v114, v115
	v_cvt_pk_bf16_f32 v114, v116, v117
	v_cvt_pk_bf16_f32 v115, v118, v119
	v_cvt_pk_bf16_f32 v116, v168, v169
	v_cvt_pk_bf16_f32 v117, v170, v171
	v_cvt_pk_bf16_f32 v118, v172, v173
	v_cvt_pk_bf16_f32 v119, v174, v175
	v_permlane32_swap_b32_e32 v217, v218
	v_permlane32_swap_b32_e32 v120, v122
	v_permlane32_swap_b32_e32 v121, v123
	v_permlane32_swap_b32_e32 v124, v126
	v_permlane32_swap_b32_e32 v125, v127
	v_permlane32_swap_b32_e32 v112, v114
	v_permlane32_swap_b32_e32 v113, v115
	v_permlane32_swap_b32_e32 v116, v118
	v_permlane32_swap_b32_e32 v117, v119
	s_add_u32 s24, s34, 0x2380c000
	s_addc_u32 s25, s35, 0
	s_add_u32 s34, s34, 0x2380e000
	s_addc_u32 s35, s35, 0
	s_add_u32 s42, s42, 0x21886000
	s_addc_u32 s43, s43, 0
	v_mov_b32_e32 v168, v201
	v_mov_b32_e32 v169, v200
	global_load_dwordx4 v[176:179], v169, s[24:25]
	global_load_dwordx4 v[172:175], v169, s[34:35]
	s_nop 0
	global_load_dwordx4 v[168:171], v168, s[42:43]
	s_and_b64 vcc, exec, s[2:3]
	s_cbranch_vccnz .LBB4_946
	s_mov_b64 s[2:3], s[8:9]
	v_mov_b32_e32 v182, v193
	global_store_dwordx2 v182, v[184:185], s[2:3] nt

; #define AT_SBAR() __builtin_amdgcn_sched_barrier(0)
; template <int OFF> DI s16x4 tr_read(int vb) { s16x4 r; asm volatile("ds_read_b64_tr_b16 %0, %1 offset:%2" : "=&v"(r) : "v"(vb), "i"(OFF) : "memory"); return r; }
; template <int D0> DI void pv_one(f32x16& od, int vb, bf16x8 pa0, bf16x8 pa1, bf16x8 pa2, bf16x8 pa3) {
;     const s16x4 l0 = tr_read<v_rd_off(D0, 0, 0)>(vb), h0 = tr_read<v_rd_off(D0, 0, 1)>(vb), l1 = tr_read<v_rd_off(D0, 1, 0)>(vb), h1 = tr_read<v_rd_off(D0, 1, 1)>(vb);
;     const s16x4 l2 = tr_read<v_rd_off(D0, 2, 0)>(vb), h2 = tr_read<v_rd_off(D0, 2, 1)>(vb), l3 = tr_read<v_rd_off(D0, 3, 0)>(vb), h3 = tr_read<v_rd_off(D0, 3, 1)>(vb);
;     asm volatile("s_waitcnt lgkmcnt(0)" ::: "memory"); AT_SBAR();
;     ...
;     od = __builtin_amdgcn_mfma_f32_32x32x16_bf16(AT_PK(l0, h0), pa0, od, 0, 0, 0);
;     od = __builtin_amdgcn_mfma_f32_32x32x16_bf16(AT_PK(l1, h1), pa1, od, 0, 0, 0);
;     od = __builtin_amdgcn_mfma_f32_32x32x16_bf16(AT_PK(l2, h2), pa2, od, 0, 0, 0);
;     od = __builtin_amdgcn_mfma_f32_32x32x16_bf16(AT_PK(l3, h3), pa3, od, 0, 0, 0);
;     ...
; }
; DI void attn_pass(const Frame& F, CvRide& cv, const bf16_t* __restrict__ Qb, const bf16_t* __restrict__ Kh, const bf16_t* __restrict__ Vh, char* lds, f32x16 (&o)[4], float& l_out, const int wave_s) {
;     ...
;     const unsigned cv_ldo = (unsigned)(((tid >> 4) * 2 * 2048 + (tid & 15) * 4) * 4), cv_sto = (unsigned)((tid >> 3) * 2048 + 8 * (tid & 7));
;     const int cv_lw = OFF_CV + (4 * (tid & 15)) * 68 + 2 * (tid >> 4), cv_lr = OFF_CV + (tid >> 3) * 68 + 8 * (tid & 7);
;     f32x4 cvA = f32x4{}, cvB = f32x4{}; unsigned cvr0 = 0, cvr1 = 0;
.LBB4_947:
	ds_read_b64_tr_b16 v[220:221], v219 offset:0x600
	ds_read_b64_tr_b16 v[222:223], v219 offset:0xe00
	ds_read_b64_tr_b16 v[224:225], v219 offset:0x1600
	ds_read_b64_tr_b16 v[226:227], v219 offset:0x1e00
	ds_read_b64_tr_b16 v[228:229], v219 offset:0x2600
	ds_read_b64_tr_b16 v[230:231], v219 offset:0x2e00
	ds_read_b64_tr_b16 v[232:233], v219 offset:0x3600
	ds_read_b64_tr_b16 v[234:235], v219 offset:0x3e00
	s_waitcnt lgkmcnt(0)
	s_nop 0
	v_mfma_f32_32x32x16_bf16 v[0:15], v[220:223], v[120:123], v[0:15]
	s_add_i32 s2, s31, 0
	v_add_u32_e32 v120, s2, v203
	s_waitcnt vmcnt(0)
	ds_write_b128 v120, v[176:179]
	s_mov_b32 s18, 0
	s_andn2_b64 vcc, exec, s[22:23]
	v_mfma_f32_32x32x16_bf16 v[0:15], v[224:227], v[124:127], v[0:15]
	v_mfma_f32_32x32x16_bf16 v[0:15], v[228:231], v[112:115], v[0:15]
	v_add_u32_e32 v112, s2, v204
	ds_write_b128 v112, v[172:175]
	v_lshl_add_u32 v112, s29, 13, v206
	ds_write_b128 v112, v[168:171] offset:49152
	s_andn2_b64 s[2:3], exec, s[22:23]
	v_mfma_f32_32x32x16_bf16 v[0:15], v[232:235], v[116:119], v[0:15]
	s_cbranch_vccnz .LBB4_952
	v_mul_f32_e32 v113, 0x44000000, v160
	v_mul_f32_e32 v114, 0x44000000, v164
	v_med3_f32 v113, v113, s28, v214
	v_med3_f32 v114, v114, s28, v214
	v_cvt_pk_fp8_f32 v115, v113, v114
	v_mul_f32_e32 v113, 0x44000000, v161
	v_mul_f32_e32 v114, 0x44000000, v165
	v_med3_f32 v113, v113, s28, v214
	v_med3_f32 v114, v114, s28, v214
	v_cvt_pk_fp8_f32 v116, v113, v114
	v_mul_f32_e32 v113, 0x44000000, v162
	v_mul_f32_e32 v114, 0x44000000, v166
	v_med3_f32 v113, v113, s28, v214
	v_med3_f32 v114, v114, s28, v214
	s_bitcmp1_b32 s58, 0
	v_cvt_pk_fp8_f32 v117, v113, v114
	v_mul_f32_e32 v113, 0x44000000, v163
	v_mul_f32_e32 v114, 0x44000000, v167
	s_cselect_b32 s8, 0x1100, 0
	v_med3_f32 v113, v113, s28, v214
	v_med3_f32 v114, v114, s28, v214
	v_cmp_eq_u32_e32 vcc, 0, v181
	v_add_u32_e32 v112, s8, v195
	v_cvt_pk_fp8_f32 v118, v113, v114
	s_and_b64 vcc, exec, vcc
	s_and_b32 s24, s58, 31
	ds_write_b16 v112, v115
	ds_write_b16 v112, v116 offset:68
	ds_write_b16 v112, v117 offset:136
	ds_write_b16 v112, v118 offset:204
	s_cbranch_vccnz .LBB4_957
	s_lshl_b32 s8, s24, 7
	s_lshl_b32 s9, s58, 6
	s_and_b32 s8, s8, 0xf00
	s_and_b32 s9, s9, 64
	s_or_b32 s18, s8, s9
	s_cbranch_execnz .LBB4_951
